# skip the K-loop's final post-MMA barrier on the last K-iteration (9 GEMM instances) so the leading half starts its epilogue while the lagging half finishes its MFMAs
# baseline (speedup 1.0000x reference)
.LBB0_229:
	s_add_i32 s73, s60, 2
	s_add_u32 s61, s58, 0xfffc0080
	s_addc_u32 s62, s59, -1
	s_add_i32 s74, 0, 0x10000
	s_cmp_eq_u32 s68, s60
	s_cselect_b32 s63, s39, s62
	s_cselect_b32 s62, s43, s61
	s_cselect_b32 s61, s47, s72
	s_cselect_b32 s60, s55, s71
	s_add_i32 s76, 0, 0x14000
	v_add_u32_e32 v156, s74, v165
	v_add_u32_e32 v166, s76, v165
	ds_read_b128 v[144:147], v156
	ds_read_b128 v[148:151], v156 offset:1024
	ds_read_b128 v[152:155], v156 offset:2048
	ds_read_b128 v[156:159], v156 offset:3072
	ds_read_b128 v[160:163], v166
	ds_read_b128 v[170:173], v166 offset:1024
	ds_read_b128 v[174:177], v166 offset:2048
	ds_read_b128 v[180:183], v166 offset:3072
	v_lshl_add_u64 v[216:217], s[58:59], 0, v[142:143]
	s_add_i32 m0, s8, 0xc000
	ds_read_b128 v[184:187], v178
	ds_read_b128 v[188:191], v178 offset:1024
	ds_read_b128 v[192:195], v178 offset:2048
	ds_read_b128 v[196:199], v178 offset:3072
	ds_read_b128 v[200:203], v178 offset:4096
	ds_read_b128 v[204:207], v178 offset:5120
	ds_read_b128 v[208:211], v178 offset:6144
	ds_read_b128 v[212:215], v178 offset:7168
	global_load_lds_dwordx4 v[216:217], off
	v_lshl_add_u64 v[216:217], s[58:59], 0, v[140:141]
	s_add_i32 m0, s8, 0xe000
	s_nop 0
	global_load_lds_dwordx4 v[216:217], off
	s_waitcnt vmcnt(8)
	s_waitcnt lgkmcnt(0)
	s_barrier
	s_setprio 1
	s_waitcnt lgkmcnt(0)
	v_mfma_f32_16x16x32_bf16 v[126:129], v[144:147], v[184:187], v[126:129]
	v_mfma_f32_16x16x32_bf16 v[122:125], v[152:155], v[184:187], v[122:125]
	v_mfma_f32_16x16x32_bf16 v[110:113], v[144:147], v[192:195], v[110:113]
	v_mfma_f32_16x16x32_bf16 v[106:109], v[152:155], v[192:195], v[106:109]
	v_mfma_f32_16x16x32_bf16 v[94:97], v[144:147], v[200:203], v[94:97]
	v_mfma_f32_16x16x32_bf16 v[90:93], v[152:155], v[200:203], v[90:93]
	v_mfma_f32_16x16x32_bf16 v[78:81], v[144:147], v[208:211], v[78:81]
	v_mfma_f32_16x16x32_bf16 v[74:77], v[152:155], v[208:211], v[74:77]
	v_mfma_f32_16x16x32_bf16 v[126:129], v[148:151], v[188:191], v[126:129]
	v_mfma_f32_16x16x32_bf16 v[122:125], v[156:159], v[188:191], v[122:125]
	v_mfma_f32_16x16x32_bf16 v[110:113], v[148:151], v[196:199], v[110:113]
	v_mfma_f32_16x16x32_bf16 v[106:109], v[156:159], v[196:199], v[106:109]
	v_mfma_f32_16x16x32_bf16 v[94:97], v[148:151], v[204:207], v[94:97]
	v_mfma_f32_16x16x32_bf16 v[90:93], v[156:159], v[204:207], v[90:93]
	v_mfma_f32_16x16x32_bf16 v[78:81], v[148:151], v[212:215], v[78:81]
	v_mfma_f32_16x16x32_bf16 v[74:77], v[156:159], v[212:215], v[74:77]
	s_setprio 0
	s_setprio 1
	v_mfma_f32_16x16x32_bf16 v[118:121], v[160:163], v[184:187], v[118:121]
	v_mfma_f32_16x16x32_bf16 v[114:117], v[174:177], v[184:187], v[114:117]
	v_mfma_f32_16x16x32_bf16 v[102:105], v[160:163], v[192:195], v[102:105]
	v_mfma_f32_16x16x32_bf16 v[98:101], v[174:177], v[192:195], v[98:101]
	v_mfma_f32_16x16x32_bf16 v[86:89], v[160:163], v[200:203], v[86:89]
	v_mfma_f32_16x16x32_bf16 v[82:85], v[174:177], v[200:203], v[82:85]
	v_mfma_f32_16x16x32_bf16 v[70:73], v[160:163], v[208:211], v[70:73]
	v_mfma_f32_16x16x32_bf16 v[66:69], v[174:177], v[208:211], v[66:69]
	v_mfma_f32_16x16x32_bf16 v[118:121], v[170:173], v[188:191], v[118:121]
	v_mfma_f32_16x16x32_bf16 v[114:117], v[180:183], v[188:191], v[114:117]
	v_mfma_f32_16x16x32_bf16 v[102:105], v[170:173], v[196:199], v[102:105]
	v_mfma_f32_16x16x32_bf16 v[98:101], v[180:183], v[196:199], v[98:101]
	v_mfma_f32_16x16x32_bf16 v[86:89], v[170:173], v[204:207], v[86:89]
	v_mfma_f32_16x16x32_bf16 v[82:85], v[180:183], v[204:207], v[82:85]
	v_mfma_f32_16x16x32_bf16 v[70:73], v[170:173], v[212:215], v[70:73]
	v_mfma_f32_16x16x32_bf16 v[66:69], v[180:183], v[212:215], v[66:69]
	s_setprio 0
	s_barrier
	s_add_i32 s74, s74, s1
	v_lshl_add_u64 v[216:217], s[60:61], 0, v[130:131]
	s_mov_b32 m0, s74
	ds_read_b128 v[184:187], v178 offset:16384
	ds_read_b128 v[188:191], v178 offset:17408
	ds_read_b128 v[192:195], v178 offset:18432
	ds_read_b128 v[196:199], v178 offset:19456
	ds_read_b128 v[200:203], v178 offset:20480
	ds_read_b128 v[204:207], v178 offset:21504
	ds_read_b128 v[208:211], v178 offset:22528
	ds_read_b128 v[212:215], v178 offset:23552
	global_load_lds_dwordx4 v[216:217], off
	s_add_i32 m0, s74, 0x2000
	s_add_u32 s74, s60, 0x40000
	v_lshl_add_u64 v[218:219], s[60:61], 0, v[132:133]
	s_addc_u32 s75, s61, 0
	s_add_i32 s76, s76, s1
	global_load_lds_dwordx4 v[218:219], off
	v_lshl_add_u64 v[220:221], s[74:75], 0, v[130:131]
	s_mov_b32 m0, s76
	v_lshl_add_u64 v[222:223], s[62:63], 0, v[136:137]
	global_load_lds_dwordx4 v[220:221], off
	v_lshl_add_u64 v[220:221], s[74:75], 0, v[132:133]
	s_add_i32 m0, s76, 0x2000
	s_nop 0
	global_load_lds_dwordx4 v[220:221], off
	v_lshl_add_u64 v[220:221], s[62:63], 0, v[134:135]
	s_mov_b32 m0, s8
	s_nop 0
	global_load_lds_dwordx4 v[220:221], off
	s_mov_b32 m0, s11
	s_nop 0
	global_load_lds_dwordx4 v[222:223], off
	s_waitcnt vmcnt(8)
	s_waitcnt lgkmcnt(0)
	s_barrier
	s_setprio 1
	s_waitcnt lgkmcnt(0)
	v_mfma_f32_16x16x32_bf16 v[62:65], v[144:147], v[184:187], v[62:65]
	v_mfma_f32_16x16x32_bf16 v[58:61], v[152:155], v[184:187], v[58:61]
	v_mfma_f32_16x16x32_bf16 v[46:49], v[144:147], v[192:195], v[46:49]
	v_mfma_f32_16x16x32_bf16 v[42:45], v[152:155], v[192:195], v[42:45]
	v_mfma_f32_16x16x32_bf16 v[30:33], v[144:147], v[200:203], v[30:33]
	v_mfma_f32_16x16x32_bf16 v[26:29], v[152:155], v[200:203], v[26:29]
	v_mfma_f32_16x16x32_bf16 v[14:17], v[144:147], v[208:211], v[14:17]
	v_mfma_f32_16x16x32_bf16 v[10:13], v[152:155], v[208:211], v[10:13]
	v_mfma_f32_16x16x32_bf16 v[62:65], v[148:151], v[188:191], v[62:65]
	v_mfma_f32_16x16x32_bf16 v[58:61], v[156:159], v[188:191], v[58:61]
	v_mfma_f32_16x16x32_bf16 v[46:49], v[148:151], v[196:199], v[46:49]
	v_mfma_f32_16x16x32_bf16 v[42:45], v[156:159], v[196:199], v[42:45]
	v_mfma_f32_16x16x32_bf16 v[30:33], v[148:151], v[204:207], v[30:33]
	v_mfma_f32_16x16x32_bf16 v[26:29], v[156:159], v[204:207], v[26:29]
	v_mfma_f32_16x16x32_bf16 v[14:17], v[148:151], v[212:215], v[14:17]
	v_mfma_f32_16x16x32_bf16 v[10:13], v[156:159], v[212:215], v[10:13]
	s_setprio 0
	s_setprio 1
	v_mfma_f32_16x16x32_bf16 v[54:57], v[160:163], v[184:187], v[54:57]
	v_mfma_f32_16x16x32_bf16 v[50:53], v[174:177], v[184:187], v[50:53]
	v_mfma_f32_16x16x32_bf16 v[38:41], v[160:163], v[192:195], v[38:41]
	v_mfma_f32_16x16x32_bf16 v[34:37], v[174:177], v[192:195], v[34:37]
	v_mfma_f32_16x16x32_bf16 v[22:25], v[160:163], v[200:203], v[22:25]
	v_mfma_f32_16x16x32_bf16 v[18:21], v[174:177], v[200:203], v[18:21]
	v_mfma_f32_16x16x32_bf16 v[6:9], v[160:163], v[208:211], v[6:9]
	v_mfma_f32_16x16x32_bf16 v[2:5], v[174:177], v[208:211], v[2:5]
	v_mfma_f32_16x16x32_bf16 v[54:57], v[170:173], v[188:191], v[54:57]
	v_mfma_f32_16x16x32_bf16 v[50:53], v[180:183], v[188:191], v[50:53]
	v_mfma_f32_16x16x32_bf16 v[38:41], v[170:173], v[196:199], v[38:41]
	v_mfma_f32_16x16x32_bf16 v[34:37], v[180:183], v[196:199], v[34:37]
	v_mfma_f32_16x16x32_bf16 v[22:25], v[170:173], v[204:207], v[22:25]
	v_mfma_f32_16x16x32_bf16 v[18:21], v[180:183], v[204:207], v[18:21]
	v_mfma_f32_16x16x32_bf16 v[6:9], v[170:173], v[212:215], v[6:9]
	v_mfma_f32_16x16x32_bf16 v[2:5], v[180:183], v[212:215], v[2:5]
	s_setprio 0
	s_barrier
	s_add_i32 s74, 0, 0x18000
	s_add_i32 s75, 0, 0x1c000
	v_add_u32_e32 v156, s74, v165
	v_add_u32_e32 v166, s75, v165
	ds_read_b128 v[144:147], v156
	ds_read_b128 v[148:151], v156 offset:1024
	ds_read_b128 v[152:155], v156 offset:2048
	ds_read_b128 v[156:159], v156 offset:3072
	ds_read_b128 v[160:163], v166
	ds_read_b128 v[170:173], v166 offset:1024
	ds_read_b128 v[174:177], v166 offset:2048
	ds_read_b128 v[180:183], v166 offset:3072
	s_add_u32 s62, s62, 0x40000
	s_addc_u32 s63, s63, 0
	s_mov_b32 m0, s16
	v_lshl_add_u64 v[232:233], s[62:63], 0, v[134:135]
	ds_read_b128 v[184:187], v178 offset:32768
	ds_read_b128 v[188:191], v178 offset:33792
	ds_read_b128 v[192:195], v178 offset:34816
	ds_read_b128 v[196:199], v178 offset:35840
	ds_read_b128 v[200:203], v178 offset:36864
	ds_read_b128 v[204:207], v178 offset:37888
	ds_read_b128 v[208:211], v178 offset:38912
	ds_read_b128 v[212:215], v178 offset:39936
	global_load_lds_dwordx4 v[232:233], off
	v_lshl_add_u64 v[232:233], s[62:63], 0, v[136:137]
	s_mov_b32 m0, s25
	s_nop 0
	global_load_lds_dwordx4 v[232:233], off
	s_waitcnt vmcnt(8)
	s_waitcnt lgkmcnt(0)
	s_barrier
	s_setprio 1
	s_waitcnt lgkmcnt(0)
	v_mfma_f32_16x16x32_bf16 v[126:129], v[144:147], v[184:187], v[126:129]
	v_mfma_f32_16x16x32_bf16 v[122:125], v[152:155], v[184:187], v[122:125]
	v_mfma_f32_16x16x32_bf16 v[110:113], v[144:147], v[192:195], v[110:113]
	v_mfma_f32_16x16x32_bf16 v[106:109], v[152:155], v[192:195], v[106:109]
	v_mfma_f32_16x16x32_bf16 v[94:97], v[144:147], v[200:203], v[94:97]
	v_mfma_f32_16x16x32_bf16 v[90:93], v[152:155], v[200:203], v[90:93]
	v_mfma_f32_16x16x32_bf16 v[78:81], v[144:147], v[208:211], v[78:81]
	v_mfma_f32_16x16x32_bf16 v[74:77], v[152:155], v[208:211], v[74:77]
	v_mfma_f32_16x16x32_bf16 v[126:129], v[148:151], v[188:191], v[126:129]
	v_mfma_f32_16x16x32_bf16 v[122:125], v[156:159], v[188:191], v[122:125]
	v_mfma_f32_16x16x32_bf16 v[110:113], v[148:151], v[196:199], v[110:113]
	v_mfma_f32_16x16x32_bf16 v[106:109], v[156:159], v[196:199], v[106:109]
	v_mfma_f32_16x16x32_bf16 v[94:97], v[148:151], v[204:207], v[94:97]
	v_mfma_f32_16x16x32_bf16 v[90:93], v[156:159], v[204:207], v[90:93]
	v_mfma_f32_16x16x32_bf16 v[78:81], v[148:151], v[212:215], v[78:81]
	v_mfma_f32_16x16x32_bf16 v[74:77], v[156:159], v[212:215], v[74:77]
	s_setprio 0
	s_setprio 1
	v_mfma_f32_16x16x32_bf16 v[118:121], v[160:163], v[184:187], v[118:121]
	v_mfma_f32_16x16x32_bf16 v[114:117], v[174:177], v[184:187], v[114:117]
	v_mfma_f32_16x16x32_bf16 v[102:105], v[160:163], v[192:195], v[102:105]
	v_mfma_f32_16x16x32_bf16 v[98:101], v[174:177], v[192:195], v[98:101]
	v_mfma_f32_16x16x32_bf16 v[86:89], v[160:163], v[200:203], v[86:89]
	v_mfma_f32_16x16x32_bf16 v[82:85], v[174:177], v[200:203], v[82:85]
	v_mfma_f32_16x16x32_bf16 v[70:73], v[160:163], v[208:211], v[70:73]
	v_mfma_f32_16x16x32_bf16 v[66:69], v[174:177], v[208:211], v[66:69]
	v_mfma_f32_16x16x32_bf16 v[118:121], v[170:173], v[188:191], v[118:121]
	v_mfma_f32_16x16x32_bf16 v[114:117], v[180:183], v[188:191], v[114:117]
	v_mfma_f32_16x16x32_bf16 v[102:105], v[170:173], v[196:199], v[102:105]
	v_mfma_f32_16x16x32_bf16 v[98:101], v[180:183], v[196:199], v[98:101]
	v_mfma_f32_16x16x32_bf16 v[86:89], v[170:173], v[204:207], v[86:89]
	v_mfma_f32_16x16x32_bf16 v[82:85], v[180:183], v[204:207], v[82:85]
	v_mfma_f32_16x16x32_bf16 v[70:73], v[170:173], v[212:215], v[70:73]
	v_mfma_f32_16x16x32_bf16 v[66:69], v[180:183], v[212:215], v[66:69]
	s_setprio 0
	s_barrier
	s_add_i32 s62, s74, s1
	v_lshl_add_u64 v[216:217], v[216:217], 0, s[56:57]
	s_mov_b32 m0, s62
	ds_read_b128 v[184:187], v178 offset:49152
	ds_read_b128 v[188:191], v178 offset:50176
	ds_read_b128 v[192:195], v178 offset:51200
	ds_read_b128 v[196:199], v178 offset:52224
	ds_read_b128 v[200:203], v178 offset:53248
	ds_read_b128 v[204:207], v178 offset:54272
	ds_read_b128 v[208:211], v178 offset:55296
	ds_read_b128 v[212:215], v178 offset:56320
	global_load_lds_dwordx4 v[216:217], off
	s_add_i32 m0, s62, 0x2000
	s_add_u32 s60, s60, 0x40080
	v_lshl_add_u64 v[216:217], v[218:219], 0, s[56:57]
	s_addc_u32 s61, s61, 0
	s_add_i32 s62, s75, s1
	global_load_lds_dwordx4 v[216:217], off
	v_lshl_add_u64 v[216:217], s[60:61], 0, v[130:131]
	s_mov_b32 m0, s62
	s_nop 0
	global_load_lds_dwordx4 v[216:217], off
	v_lshl_add_u64 v[216:217], s[60:61], 0, v[132:133]
	s_add_i32 m0, s62, 0x2000
	s_nop 0
	global_load_lds_dwordx4 v[216:217], off
	v_lshl_add_u64 v[216:217], v[220:221], 0, s[56:57]
	s_mov_b32 m0, s64
	s_nop 0
	global_load_lds_dwordx4 v[216:217], off
	v_lshl_add_u64 v[216:217], v[222:223], 0, s[56:57]
	s_mov_b32 m0, s65
	s_nop 0
	global_load_lds_dwordx4 v[216:217], off
	s_waitcnt vmcnt(8)
	s_waitcnt lgkmcnt(0)
	s_barrier
	s_setprio 1
	s_waitcnt lgkmcnt(0)
	v_mfma_f32_16x16x32_bf16 v[62:65], v[144:147], v[184:187], v[62:65]
	v_mfma_f32_16x16x32_bf16 v[58:61], v[152:155], v[184:187], v[58:61]
	v_mfma_f32_16x16x32_bf16 v[46:49], v[144:147], v[192:195], v[46:49]
	v_mfma_f32_16x16x32_bf16 v[42:45], v[152:155], v[192:195], v[42:45]
	v_mfma_f32_16x16x32_bf16 v[30:33], v[144:147], v[200:203], v[30:33]
	v_mfma_f32_16x16x32_bf16 v[26:29], v[152:155], v[200:203], v[26:29]
	v_mfma_f32_16x16x32_bf16 v[14:17], v[144:147], v[208:211], v[14:17]
	v_mfma_f32_16x16x32_bf16 v[10:13], v[152:155], v[208:211], v[10:13]
	v_mfma_f32_16x16x32_bf16 v[62:65], v[148:151], v[188:191], v[62:65]
	v_mfma_f32_16x16x32_bf16 v[58:61], v[156:159], v[188:191], v[58:61]
	v_mfma_f32_16x16x32_bf16 v[46:49], v[148:151], v[196:199], v[46:49]
	v_mfma_f32_16x16x32_bf16 v[42:45], v[156:159], v[196:199], v[42:45]
	v_mfma_f32_16x16x32_bf16 v[30:33], v[148:151], v[204:207], v[30:33]
	v_mfma_f32_16x16x32_bf16 v[26:29], v[156:159], v[204:207], v[26:29]
	v_mfma_f32_16x16x32_bf16 v[14:17], v[148:151], v[212:215], v[14:17]
	v_mfma_f32_16x16x32_bf16 v[10:13], v[156:159], v[212:215], v[10:13]
	s_setprio 0
	s_setprio 1
	v_mfma_f32_16x16x32_bf16 v[54:57], v[160:163], v[184:187], v[54:57]
	v_mfma_f32_16x16x32_bf16 v[50:53], v[174:177], v[184:187], v[50:53]
	v_mfma_f32_16x16x32_bf16 v[38:41], v[160:163], v[192:195], v[38:41]
	v_mfma_f32_16x16x32_bf16 v[34:37], v[174:177], v[192:195], v[34:37]
	v_mfma_f32_16x16x32_bf16 v[22:25], v[160:163], v[200:203], v[22:25]
	v_mfma_f32_16x16x32_bf16 v[18:21], v[174:177], v[200:203], v[18:21]
	v_mfma_f32_16x16x32_bf16 v[6:9], v[160:163], v[208:211], v[6:9]
	v_mfma_f32_16x16x32_bf16 v[2:5], v[174:177], v[208:211], v[2:5]
	v_mfma_f32_16x16x32_bf16 v[54:57], v[170:173], v[188:191], v[54:57]
	v_mfma_f32_16x16x32_bf16 v[50:53], v[180:183], v[188:191], v[50:53]
	v_mfma_f32_16x16x32_bf16 v[38:41], v[170:173], v[196:199], v[38:41]
	v_mfma_f32_16x16x32_bf16 v[34:37], v[180:183], v[196:199], v[34:37]
	v_mfma_f32_16x16x32_bf16 v[22:25], v[170:173], v[204:207], v[22:25]
	v_mfma_f32_16x16x32_bf16 v[18:21], v[180:183], v[204:207], v[18:21]
	v_mfma_f32_16x16x32_bf16 v[6:9], v[170:173], v[212:215], v[6:9]
	v_mfma_f32_16x16x32_bf16 v[2:5], v[180:183], v[212:215], v[2:5]
	s_setprio 0
	s_add_u32 s71, s71, 0x100
	s_addc_u32 s72, s72, 0
	s_add_u32 s58, s58, 0x100
	s_addc_u32 s59, s59, 0
	s_cmp_ge_i32 s73, s0
	s_mov_b32 s60, s73
	s_cbranch_scc1 .Lq4skip_ph1b
	s_barrier
	s_branch .LBB0_229
.Lq4skip_ph1b:
	s_nop 1
	s_mov_b64 s[72:73], 0xe800000
	v_mov_b32_e32 v209, v1
	s_and_b64 vcc, exec, s[34:35]
	s_cbranch_vccz .LBB0_232

.LBB0_298:
	s_add_i32 s71, s58, 2
	s_add_u32 s59, s54, 0xfffe0080
	s_addc_u32 s60, s55, -1
	s_add_i32 s72, 0, 0x10000
	s_cmp_eq_u32 s65, s58
	s_cselect_b32 s61, s39, s60
	s_cselect_b32 s60, s41, s59
	s_cselect_b32 s59, s43, s70
	s_cselect_b32 s58, s53, s69
	s_add_i32 s73, 0, 0x14000
	v_add_u32_e32 v2, s72, v198
	v_add_u32_e32 v6, s73, v198
	ds_read_b128 v[26:29], v2
	ds_read_b128 v[30:33], v2 offset:1024
	ds_read_b128 v[18:21], v2 offset:2048
	ds_read_b128 v[22:25], v2 offset:3072
	ds_read_b128 v[10:13], v6
	ds_read_b128 v[14:17], v6 offset:1024
	ds_read_b128 v[2:5], v6 offset:2048
	ds_read_b128 v[6:9], v6 offset:3072
	v_lshl_add_u64 v[170:171], s[54:55], 0, v[186:187]
	s_add_i32 m0, s8, 0xc000
	ds_read_b128 v[188:191], v200
	ds_read_b128 v[192:195], v200 offset:1024
	ds_read_b128 v[202:205], v200 offset:2048
	ds_read_b128 v[206:209], v200 offset:3072
	ds_read_b128 v[210:213], v200 offset:4096
	ds_read_b128 v[214:217], v200 offset:5120
	ds_read_b128 v[236:239], v200 offset:6144
	ds_read_b128 v[240:243], v200 offset:7168
	global_load_lds_dwordx4 v[170:171], off
	v_lshl_add_u64 v[170:171], s[54:55], 0, v[184:185]
	s_add_i32 m0, s8, 0xe000
	s_nop 0
	global_load_lds_dwordx4 v[170:171], off
	s_waitcnt vmcnt(8)
	s_waitcnt lgkmcnt(0)
	s_barrier
	s_setprio 1
	s_waitcnt lgkmcnt(0)
	v_mfma_scale_f32_16x16x128_f8f6f4 v[158:161], v[26:33], v[188:195], v[158:161], v196, v169 op_sel_hi:[0,0,0]
	v_mfma_scale_f32_16x16x128_f8f6f4 v[154:157], v[18:25], v[188:195], v[154:157], v196, v169 op_sel_hi:[0,0,0]
	v_mfma_scale_f32_16x16x128_f8f6f4 v[142:145], v[26:33], v[202:209], v[142:145], v196, v169 op_sel_hi:[0,0,0]
	v_mfma_scale_f32_16x16x128_f8f6f4 v[138:141], v[18:25], v[202:209], v[138:141], v196, v169 op_sel_hi:[0,0,0]
	v_mfma_scale_f32_16x16x128_f8f6f4 v[126:129], v[26:33], v[210:217], v[126:129], v196, v169 op_sel_hi:[0,0,0]
	v_mfma_scale_f32_16x16x128_f8f6f4 v[122:125], v[18:25], v[210:217], v[122:125], v196, v169 op_sel_hi:[0,0,0]
	v_mfma_scale_f32_16x16x128_f8f6f4 v[110:113], v[26:33], v[236:243], v[110:113], v196, v169 op_sel_hi:[0,0,0]
	v_mfma_scale_f32_16x16x128_f8f6f4 v[106:109], v[18:25], v[236:243], v[106:109], v196, v169 op_sel_hi:[0,0,0]
	s_setprio 0
	s_setprio 1
	v_mfma_scale_f32_16x16x128_f8f6f4 v[150:153], v[10:17], v[188:195], v[150:153], v196, v169 op_sel_hi:[0,0,0]
	v_mfma_scale_f32_16x16x128_f8f6f4 v[146:149], v[2:9], v[188:195], v[146:149], v196, v169 op_sel_hi:[0,0,0]
	v_mfma_scale_f32_16x16x128_f8f6f4 v[134:137], v[10:17], v[202:209], v[134:137], v196, v169 op_sel_hi:[0,0,0]
	v_mfma_scale_f32_16x16x128_f8f6f4 v[130:133], v[2:9], v[202:209], v[130:133], v196, v169 op_sel_hi:[0,0,0]
	v_mfma_scale_f32_16x16x128_f8f6f4 v[118:121], v[10:17], v[210:217], v[118:121], v196, v169 op_sel_hi:[0,0,0]
	v_mfma_scale_f32_16x16x128_f8f6f4 v[114:117], v[2:9], v[210:217], v[114:117], v196, v169 op_sel_hi:[0,0,0]
	v_mfma_scale_f32_16x16x128_f8f6f4 v[102:105], v[10:17], v[236:243], v[102:105], v196, v169 op_sel_hi:[0,0,0]
	v_mfma_scale_f32_16x16x128_f8f6f4 v[98:101], v[2:9], v[236:243], v[98:101], v196, v169 op_sel_hi:[0,0,0]
	s_setprio 0
	s_barrier
	s_add_i32 s72, s72, s1
	v_lshl_add_u64 v[188:189], s[58:59], 0, v[162:163]
	s_mov_b32 m0, s72
	ds_read_b128 v[202:205], v200 offset:16384
	ds_read_b128 v[206:209], v200 offset:17408
	ds_read_b128 v[210:213], v200 offset:18432
	ds_read_b128 v[214:217], v200 offset:19456
	ds_read_b128 v[236:239], v200 offset:20480
	ds_read_b128 v[240:243], v200 offset:21504
	ds_read_b128 v[244:247], v200 offset:22528
	ds_read_b128 v[248:251], v200 offset:23552
	global_load_lds_dwordx4 v[188:189], off
	s_add_i32 m0, s72, 0x2000
	s_add_u32 s74, s58, 0x20000
	v_lshl_add_u64 v[190:191], s[58:59], 0, v[164:165]
	s_addc_u32 s75, s59, 0
	s_add_i32 s72, s73, s1
	global_load_lds_dwordx4 v[190:191], off
	v_lshl_add_u64 v[170:171], s[74:75], 0, v[162:163]
	s_mov_b32 m0, s72
	v_lshl_add_u64 v[192:193], s[60:61], 0, v[178:179]
	global_load_lds_dwordx4 v[170:171], off
	v_lshl_add_u64 v[170:171], s[74:75], 0, v[164:165]
	s_add_i32 m0, s72, 0x2000
	v_lshl_add_u64 v[194:195], s[60:61], 0, v[180:181]
	global_load_lds_dwordx4 v[170:171], off
	s_mov_b32 m0, s8
	s_nop 0
	global_load_lds_dwordx4 v[192:193], off
	s_mov_b32 m0, s11
	s_nop 0
	global_load_lds_dwordx4 v[194:195], off
	s_waitcnt vmcnt(8)
	s_waitcnt lgkmcnt(0)
	s_barrier
	s_setprio 1
	s_waitcnt lgkmcnt(0)
	v_mfma_scale_f32_16x16x128_f8f6f4 v[94:97], v[26:33], v[202:209], v[94:97], v196, v169 op_sel_hi:[0,0,0]
	v_mfma_scale_f32_16x16x128_f8f6f4 v[90:93], v[18:25], v[202:209], v[90:93], v196, v169 op_sel_hi:[0,0,0]
	v_mfma_scale_f32_16x16x128_f8f6f4 v[78:81], v[26:33], v[210:217], v[78:81], v196, v169 op_sel_hi:[0,0,0]
	v_mfma_scale_f32_16x16x128_f8f6f4 v[74:77], v[18:25], v[210:217], v[74:77], v196, v169 op_sel_hi:[0,0,0]
	v_mfma_scale_f32_16x16x128_f8f6f4 v[62:65], v[26:33], v[236:243], v[62:65], v196, v169 op_sel_hi:[0,0,0]
	v_mfma_scale_f32_16x16x128_f8f6f4 v[58:61], v[18:25], v[236:243], v[58:61], v196, v169 op_sel_hi:[0,0,0]
	v_mfma_scale_f32_16x16x128_f8f6f4 v[46:49], v[26:33], v[244:251], v[46:49], v196, v169 op_sel_hi:[0,0,0]
	v_mfma_scale_f32_16x16x128_f8f6f4 v[42:45], v[18:25], v[244:251], v[42:45], v196, v169 op_sel_hi:[0,0,0]
	s_setprio 0
	s_setprio 1
	v_mfma_scale_f32_16x16x128_f8f6f4 v[86:89], v[10:17], v[202:209], v[86:89], v196, v169 op_sel_hi:[0,0,0]
	v_mfma_scale_f32_16x16x128_f8f6f4 v[82:85], v[2:9], v[202:209], v[82:85], v196, v169 op_sel_hi:[0,0,0]
	v_mfma_scale_f32_16x16x128_f8f6f4 v[70:73], v[10:17], v[210:217], v[70:73], v196, v169 op_sel_hi:[0,0,0]
	v_mfma_scale_f32_16x16x128_f8f6f4 v[66:69], v[2:9], v[210:217], v[66:69], v196, v169 op_sel_hi:[0,0,0]
	v_mfma_scale_f32_16x16x128_f8f6f4 v[54:57], v[10:17], v[236:243], v[54:57], v196, v169 op_sel_hi:[0,0,0]
	v_mfma_scale_f32_16x16x128_f8f6f4 v[50:53], v[2:9], v[236:243], v[50:53], v196, v169 op_sel_hi:[0,0,0]
	v_mfma_scale_f32_16x16x128_f8f6f4 v[38:41], v[10:17], v[244:251], v[38:41], v196, v169 op_sel_hi:[0,0,0]
	v_mfma_scale_f32_16x16x128_f8f6f4 v[34:37], v[2:9], v[244:251], v[34:37], v196, v169 op_sel_hi:[0,0,0]
	s_setprio 0
	s_barrier
	s_add_i32 s72, 0, 0x18000
	s_add_i32 s73, 0, 0x1c000
	v_add_u32_e32 v2, s72, v198
	v_add_u32_e32 v6, s73, v198
	ds_read_b128 v[26:29], v2
	ds_read_b128 v[30:33], v2 offset:1024
	ds_read_b128 v[18:21], v2 offset:2048
	ds_read_b128 v[22:25], v2 offset:3072
	ds_read_b128 v[10:13], v6
	ds_read_b128 v[14:17], v6 offset:1024
	ds_read_b128 v[2:5], v6 offset:2048
	ds_read_b128 v[6:9], v6 offset:3072
	s_add_u32 s60, s60, 0x20000
	s_addc_u32 s61, s61, 0
	s_mov_b32 m0, s16
	v_lshl_add_u64 v[170:171], s[60:61], 0, v[178:179]
	ds_read_b128 v[202:205], v200 offset:32768
	ds_read_b128 v[206:209], v200 offset:33792
	ds_read_b128 v[210:213], v200 offset:34816
	ds_read_b128 v[214:217], v200 offset:35840
	ds_read_b128 v[236:239], v200 offset:36864
	ds_read_b128 v[240:243], v200 offset:37888
	ds_read_b128 v[244:247], v200 offset:38912
	ds_read_b128 v[248:251], v200 offset:39936
	global_load_lds_dwordx4 v[170:171], off
	v_lshl_add_u64 v[170:171], s[60:61], 0, v[180:181]
	s_mov_b32 m0, s25
	s_nop 0
	global_load_lds_dwordx4 v[170:171], off
	s_waitcnt vmcnt(8)
	s_waitcnt lgkmcnt(0)
	s_barrier
	s_setprio 1
	s_waitcnt lgkmcnt(0)
	v_mfma_scale_f32_16x16x128_f8f6f4 v[158:161], v[26:33], v[202:209], v[158:161], v196, v169 op_sel_hi:[0,0,0]
	v_mfma_scale_f32_16x16x128_f8f6f4 v[154:157], v[18:25], v[202:209], v[154:157], v196, v169 op_sel_hi:[0,0,0]
	v_mfma_scale_f32_16x16x128_f8f6f4 v[142:145], v[26:33], v[210:217], v[142:145], v196, v169 op_sel_hi:[0,0,0]
	v_mfma_scale_f32_16x16x128_f8f6f4 v[138:141], v[18:25], v[210:217], v[138:141], v196, v169 op_sel_hi:[0,0,0]
	v_mfma_scale_f32_16x16x128_f8f6f4 v[126:129], v[26:33], v[236:243], v[126:129], v196, v169 op_sel_hi:[0,0,0]
	v_mfma_scale_f32_16x16x128_f8f6f4 v[122:125], v[18:25], v[236:243], v[122:125], v196, v169 op_sel_hi:[0,0,0]
	v_mfma_scale_f32_16x16x128_f8f6f4 v[110:113], v[26:33], v[244:251], v[110:113], v196, v169 op_sel_hi:[0,0,0]
	v_mfma_scale_f32_16x16x128_f8f6f4 v[106:109], v[18:25], v[244:251], v[106:109], v196, v169 op_sel_hi:[0,0,0]
	s_setprio 0
	s_setprio 1
	v_mfma_scale_f32_16x16x128_f8f6f4 v[150:153], v[10:17], v[202:209], v[150:153], v196, v169 op_sel_hi:[0,0,0]
	v_mfma_scale_f32_16x16x128_f8f6f4 v[146:149], v[2:9], v[202:209], v[146:149], v196, v169 op_sel_hi:[0,0,0]
	v_mfma_scale_f32_16x16x128_f8f6f4 v[134:137], v[10:17], v[210:217], v[134:137], v196, v169 op_sel_hi:[0,0,0]
	v_mfma_scale_f32_16x16x128_f8f6f4 v[130:133], v[2:9], v[210:217], v[130:133], v196, v169 op_sel_hi:[0,0,0]
	v_mfma_scale_f32_16x16x128_f8f6f4 v[118:121], v[10:17], v[236:243], v[118:121], v196, v169 op_sel_hi:[0,0,0]
	v_mfma_scale_f32_16x16x128_f8f6f4 v[114:117], v[2:9], v[236:243], v[114:117], v196, v169 op_sel_hi:[0,0,0]
	v_mfma_scale_f32_16x16x128_f8f6f4 v[102:105], v[10:17], v[244:251], v[102:105], v196, v169 op_sel_hi:[0,0,0]
	v_mfma_scale_f32_16x16x128_f8f6f4 v[98:101], v[2:9], v[244:251], v[98:101], v196, v169 op_sel_hi:[0,0,0]
	s_setprio 0
	s_barrier
	s_add_i32 s60, s72, s1
	v_lshl_add_u64 v[170:171], v[188:189], 0, s[56:57]
	s_mov_b32 m0, s60
	ds_read_b128 v[202:205], v200 offset:49152
	ds_read_b128 v[206:209], v200 offset:50176
	ds_read_b128 v[210:213], v200 offset:51200
	ds_read_b128 v[214:217], v200 offset:52224
	ds_read_b128 v[236:239], v200 offset:53248
	ds_read_b128 v[240:243], v200 offset:54272
	ds_read_b128 v[244:247], v200 offset:55296
	ds_read_b128 v[248:251], v200 offset:56320
	global_load_lds_dwordx4 v[170:171], off
	s_add_i32 m0, s60, 0x2000
	s_add_u32 s58, s58, 0x20080
	v_lshl_add_u64 v[170:171], v[190:191], 0, s[56:57]
	s_addc_u32 s59, s59, 0
	s_add_i32 s60, s73, s1
	global_load_lds_dwordx4 v[170:171], off
	v_lshl_add_u64 v[170:171], s[58:59], 0, v[162:163]
	s_mov_b32 m0, s60
	s_nop 0
	global_load_lds_dwordx4 v[170:171], off
	v_lshl_add_u64 v[170:171], s[58:59], 0, v[164:165]
	s_add_i32 m0, s60, 0x2000
	s_nop 0
	global_load_lds_dwordx4 v[170:171], off
	v_lshl_add_u64 v[170:171], v[192:193], 0, s[56:57]
	s_mov_b32 m0, s62
	s_nop 0
	global_load_lds_dwordx4 v[170:171], off
	v_lshl_add_u64 v[170:171], v[194:195], 0, s[56:57]
	s_mov_b32 m0, s63
	s_nop 0
	global_load_lds_dwordx4 v[170:171], off
	s_waitcnt vmcnt(8)
	s_waitcnt lgkmcnt(0)
	s_barrier
	s_setprio 1
	s_waitcnt lgkmcnt(0)
	v_mfma_scale_f32_16x16x128_f8f6f4 v[94:97], v[26:33], v[202:209], v[94:97], v196, v169 op_sel_hi:[0,0,0]
	v_mfma_scale_f32_16x16x128_f8f6f4 v[90:93], v[18:25], v[202:209], v[90:93], v196, v169 op_sel_hi:[0,0,0]
	v_mfma_scale_f32_16x16x128_f8f6f4 v[78:81], v[26:33], v[210:217], v[78:81], v196, v169 op_sel_hi:[0,0,0]
	v_mfma_scale_f32_16x16x128_f8f6f4 v[74:77], v[18:25], v[210:217], v[74:77], v196, v169 op_sel_hi:[0,0,0]
	v_mfma_scale_f32_16x16x128_f8f6f4 v[62:65], v[26:33], v[236:243], v[62:65], v196, v169 op_sel_hi:[0,0,0]
	v_mfma_scale_f32_16x16x128_f8f6f4 v[58:61], v[18:25], v[236:243], v[58:61], v196, v169 op_sel_hi:[0,0,0]
	v_mfma_scale_f32_16x16x128_f8f6f4 v[46:49], v[26:33], v[244:251], v[46:49], v196, v169 op_sel_hi:[0,0,0]
	v_mfma_scale_f32_16x16x128_f8f6f4 v[42:45], v[18:25], v[244:251], v[42:45], v196, v169 op_sel_hi:[0,0,0]
	s_setprio 0
	s_setprio 1
	v_mfma_scale_f32_16x16x128_f8f6f4 v[86:89], v[10:17], v[202:209], v[86:89], v196, v169 op_sel_hi:[0,0,0]
	v_mfma_scale_f32_16x16x128_f8f6f4 v[82:85], v[2:9], v[202:209], v[82:85], v196, v169 op_sel_hi:[0,0,0]
	v_mfma_scale_f32_16x16x128_f8f6f4 v[70:73], v[10:17], v[210:217], v[70:73], v196, v169 op_sel_hi:[0,0,0]
	v_mfma_scale_f32_16x16x128_f8f6f4 v[66:69], v[2:9], v[210:217], v[66:69], v196, v169 op_sel_hi:[0,0,0]
	v_mfma_scale_f32_16x16x128_f8f6f4 v[54:57], v[10:17], v[236:243], v[54:57], v196, v169 op_sel_hi:[0,0,0]
	v_mfma_scale_f32_16x16x128_f8f6f4 v[50:53], v[2:9], v[236:243], v[50:53], v196, v169 op_sel_hi:[0,0,0]
	v_mfma_scale_f32_16x16x128_f8f6f4 v[38:41], v[10:17], v[244:251], v[38:41], v196, v169 op_sel_hi:[0,0,0]
	v_mfma_scale_f32_16x16x128_f8f6f4 v[34:37], v[2:9], v[244:251], v[34:37], v196, v169 op_sel_hi:[0,0,0]
	s_setprio 0
	s_add_u32 s69, s69, 0x100
	s_addc_u32 s70, s70, 0
	s_add_u32 s54, s54, 0x100
	s_addc_u32 s55, s55, 0
	s_cmp_ge_i32 s71, s0
	s_mov_b32 s58, s71
	s_cbranch_scc1 .Lq4skip_ph1f
	s_barrier
	s_branch .LBB0_298
.Lq4skip_ph1f:
	s_nop 1
	s_mov_b64 s[72:73], 0xe800000
	s_mov_b64 s[70:71], 0xe800800
	v_mov_b32_e32 v209, v1
	s_and_b64 vcc, exec, s[34:35]
	s_cbranch_vccz .LBB0_301

.LBB0_469:
	s_add_i32 s73, s68, 2
	s_add_u32 s69, s64, 0xfffc0080
	s_addc_u32 s70, s65, -1
	s_add_i32 s74, 0, 0x10000
	s_cmp_eq_u32 s24, s68
	s_cselect_b32 s71, s59, s70
	s_cselect_b32 s70, s58, s69
	s_cselect_b32 s69, s51, s72
	s_cselect_b32 s68, s53, s66
	s_add_i32 s76, 0, 0x14000
	v_add_u32_e32 v152, s74, v220
	v_add_u32_e32 v164, s76, v220
	ds_read_b128 v[106:109], v152
	ds_read_b128 v[110:113], v152 offset:1024
	ds_read_b128 v[114:117], v152 offset:2048
	ds_read_b128 v[152:155], v152 offset:3072
	ds_read_b128 v[156:159], v164
	ds_read_b128 v[160:163], v164 offset:1024
	ds_read_b128 v[170:173], v164 offset:2048
	ds_read_b128 v[174:177], v164 offset:3072
	v_lshl_add_u64 v[164:165], s[64:65], 0, v[150:151]
	s_add_i32 m0, s14, 0xc000
	ds_read_b128 v[178:181], v222
	ds_read_b128 v[182:185], v222 offset:1024
	ds_read_b128 v[186:189], v222 offset:2048
	ds_read_b128 v[190:193], v222 offset:3072
	ds_read_b128 v[194:197], v222 offset:4096
	ds_read_b128 v[198:201], v222 offset:5120
	ds_read_b128 v[202:205], v222 offset:6144
	ds_read_b128 v[206:209], v222 offset:7168
	global_load_lds_dwordx4 v[164:165], off
	v_lshl_add_u64 v[164:165], s[64:65], 0, v[148:149]
	s_add_i32 m0, s14, 0xe000
	s_nop 0
	global_load_lds_dwordx4 v[164:165], off
	s_waitcnt vmcnt(8)
	s_waitcnt lgkmcnt(0)
	s_barrier
	s_setprio 1
	s_waitcnt lgkmcnt(0)
	v_mfma_f32_16x16x32_bf16 v[138:141], v[106:109], v[178:181], v[138:141]
	v_mfma_f32_16x16x32_bf16 v[62:65], v[114:117], v[178:181], v[62:65]
	v_mfma_f32_16x16x32_bf16 v[130:133], v[106:109], v[186:189], v[130:133]
	v_mfma_f32_16x16x32_bf16 v[54:57], v[114:117], v[186:189], v[54:57]
	v_mfma_f32_16x16x32_bf16 v[122:125], v[106:109], v[194:197], v[122:125]
	v_mfma_f32_16x16x32_bf16 v[46:49], v[114:117], v[194:197], v[46:49]
	v_mfma_f32_16x16x32_bf16 v[102:105], v[106:109], v[202:205], v[102:105]
	v_mfma_f32_16x16x32_bf16 v[38:41], v[114:117], v[202:205], v[38:41]
	v_mfma_f32_16x16x32_bf16 v[138:141], v[110:113], v[182:185], v[138:141]
	v_mfma_f32_16x16x32_bf16 v[62:65], v[152:155], v[182:185], v[62:65]
	v_mfma_f32_16x16x32_bf16 v[130:133], v[110:113], v[190:193], v[130:133]
	v_mfma_f32_16x16x32_bf16 v[54:57], v[152:155], v[190:193], v[54:57]
	v_mfma_f32_16x16x32_bf16 v[122:125], v[110:113], v[198:201], v[122:125]
	v_mfma_f32_16x16x32_bf16 v[46:49], v[152:155], v[198:201], v[46:49]
	v_mfma_f32_16x16x32_bf16 v[102:105], v[110:113], v[206:209], v[102:105]
	v_mfma_f32_16x16x32_bf16 v[38:41], v[152:155], v[206:209], v[38:41]
	s_setprio 0
	s_setprio 1
	v_mfma_f32_16x16x32_bf16 v[134:137], v[156:159], v[178:181], v[134:137]
	v_mfma_f32_16x16x32_bf16 v[58:61], v[170:173], v[178:181], v[58:61]
	v_mfma_f32_16x16x32_bf16 v[126:129], v[156:159], v[186:189], v[126:129]
	v_mfma_f32_16x16x32_bf16 v[50:53], v[170:173], v[186:189], v[50:53]
	v_mfma_f32_16x16x32_bf16 v[118:121], v[156:159], v[194:197], v[118:121]
	v_mfma_f32_16x16x32_bf16 v[42:45], v[170:173], v[194:197], v[42:45]
	v_mfma_f32_16x16x32_bf16 v[98:101], v[156:159], v[202:205], v[98:101]
	v_mfma_f32_16x16x32_bf16 v[34:37], v[170:173], v[202:205], v[34:37]
	v_mfma_f32_16x16x32_bf16 v[134:137], v[160:163], v[182:185], v[134:137]
	v_mfma_f32_16x16x32_bf16 v[58:61], v[174:177], v[182:185], v[58:61]
	v_mfma_f32_16x16x32_bf16 v[126:129], v[160:163], v[190:193], v[126:129]
	v_mfma_f32_16x16x32_bf16 v[50:53], v[174:177], v[190:193], v[50:53]
	v_mfma_f32_16x16x32_bf16 v[118:121], v[160:163], v[198:201], v[118:121]
	v_mfma_f32_16x16x32_bf16 v[42:45], v[174:177], v[198:201], v[42:45]
	v_mfma_f32_16x16x32_bf16 v[98:101], v[160:163], v[206:209], v[98:101]
	v_mfma_f32_16x16x32_bf16 v[34:37], v[174:177], v[206:209], v[34:37]
	s_setprio 0
	s_barrier
	s_add_i32 s74, s74, s13
	v_lshl_add_u64 v[164:165], s[68:69], 0, v[166:167]
	s_mov_b32 m0, s74
	ds_read_b128 v[178:181], v222 offset:16384
	ds_read_b128 v[182:185], v222 offset:17408
	ds_read_b128 v[186:189], v222 offset:18432
	ds_read_b128 v[190:193], v222 offset:19456
	ds_read_b128 v[194:197], v222 offset:20480
	ds_read_b128 v[198:201], v222 offset:21504
	ds_read_b128 v[202:205], v222 offset:22528
	ds_read_b128 v[206:209], v222 offset:23552
	global_load_lds_dwordx4 v[164:165], off
	s_add_i32 m0, s74, 0x2000
	s_add_u32 s74, s68, 0x8000
	v_lshl_add_u64 v[210:211], s[68:69], 0, v[142:143]
	s_addc_u32 s75, s69, 0
	s_add_i32 s76, s76, s13
	global_load_lds_dwordx4 v[210:211], off
	v_lshl_add_u64 v[212:213], s[74:75], 0, v[166:167]
	s_mov_b32 m0, s76
	v_lshl_add_u64 v[214:215], s[70:71], 0, v[146:147]
	global_load_lds_dwordx4 v[212:213], off
	v_lshl_add_u64 v[212:213], s[74:75], 0, v[142:143]
	s_add_i32 m0, s76, 0x2000
	s_nop 0
	global_load_lds_dwordx4 v[212:213], off
	v_lshl_add_u64 v[212:213], s[70:71], 0, v[144:145]
	s_mov_b32 m0, s14
	s_nop 0
	global_load_lds_dwordx4 v[212:213], off
	s_mov_b32 m0, s15
	s_nop 0
	global_load_lds_dwordx4 v[214:215], off
	s_waitcnt vmcnt(8)
	s_waitcnt lgkmcnt(0)
	s_barrier
	s_setprio 1
	s_waitcnt lgkmcnt(0)
	v_mfma_f32_16x16x32_bf16 v[94:97], v[106:109], v[178:181], v[94:97]
	v_mfma_f32_16x16x32_bf16 v[30:33], v[114:117], v[178:181], v[30:33]
	v_mfma_f32_16x16x32_bf16 v[86:89], v[106:109], v[186:189], v[86:89]
	v_mfma_f32_16x16x32_bf16 v[22:25], v[114:117], v[186:189], v[22:25]
	v_mfma_f32_16x16x32_bf16 v[78:81], v[106:109], v[194:197], v[78:81]
	v_mfma_f32_16x16x32_bf16 v[14:17], v[114:117], v[194:197], v[14:17]
	v_mfma_f32_16x16x32_bf16 v[70:73], v[106:109], v[202:205], v[70:73]
	v_mfma_f32_16x16x32_bf16 v[6:9], v[114:117], v[202:205], v[6:9]
	v_mfma_f32_16x16x32_bf16 v[94:97], v[110:113], v[182:185], v[94:97]
	v_mfma_f32_16x16x32_bf16 v[30:33], v[152:155], v[182:185], v[30:33]
	v_mfma_f32_16x16x32_bf16 v[86:89], v[110:113], v[190:193], v[86:89]
	v_mfma_f32_16x16x32_bf16 v[22:25], v[152:155], v[190:193], v[22:25]
	v_mfma_f32_16x16x32_bf16 v[78:81], v[110:113], v[198:201], v[78:81]
	v_mfma_f32_16x16x32_bf16 v[14:17], v[152:155], v[198:201], v[14:17]
	v_mfma_f32_16x16x32_bf16 v[70:73], v[110:113], v[206:209], v[70:73]
	v_mfma_f32_16x16x32_bf16 v[6:9], v[152:155], v[206:209], v[6:9]
	s_setprio 0
	s_setprio 1
	v_mfma_f32_16x16x32_bf16 v[90:93], v[156:159], v[178:181], v[90:93]
	v_mfma_f32_16x16x32_bf16 v[26:29], v[170:173], v[178:181], v[26:29]
	v_mfma_f32_16x16x32_bf16 v[82:85], v[156:159], v[186:189], v[82:85]
	v_mfma_f32_16x16x32_bf16 v[18:21], v[170:173], v[186:189], v[18:21]
	v_mfma_f32_16x16x32_bf16 v[74:77], v[156:159], v[194:197], v[74:77]
	v_mfma_f32_16x16x32_bf16 v[10:13], v[170:173], v[194:197], v[10:13]
	v_mfma_f32_16x16x32_bf16 v[66:69], v[156:159], v[202:205], v[66:69]
	v_mfma_f32_16x16x32_bf16 v[2:5], v[170:173], v[202:205], v[2:5]
	v_mfma_f32_16x16x32_bf16 v[90:93], v[160:163], v[182:185], v[90:93]
	v_mfma_f32_16x16x32_bf16 v[26:29], v[174:177], v[182:185], v[26:29]
	v_mfma_f32_16x16x32_bf16 v[82:85], v[160:163], v[190:193], v[82:85]
	v_mfma_f32_16x16x32_bf16 v[18:21], v[174:177], v[190:193], v[18:21]
	v_mfma_f32_16x16x32_bf16 v[74:77], v[160:163], v[198:201], v[74:77]
	v_mfma_f32_16x16x32_bf16 v[10:13], v[174:177], v[198:201], v[10:13]
	v_mfma_f32_16x16x32_bf16 v[66:69], v[160:163], v[206:209], v[66:69]
	v_mfma_f32_16x16x32_bf16 v[2:5], v[174:177], v[206:209], v[2:5]
	s_setprio 0
	s_barrier
	s_add_i32 s74, 0, 0x18000
	s_add_i32 s75, 0, 0x1c000
	v_add_u32_e32 v152, s74, v220
	v_add_u32_e32 v174, s75, v220
	ds_read_b128 v[106:109], v152
	ds_read_b128 v[110:113], v152 offset:1024
	ds_read_b128 v[114:117], v152 offset:2048
	ds_read_b128 v[152:155], v152 offset:3072
	ds_read_b128 v[156:159], v174
	ds_read_b128 v[160:163], v174 offset:1024
	ds_read_b128 v[170:173], v174 offset:2048
	ds_read_b128 v[174:177], v174 offset:3072
	s_add_u32 s70, s70, 0x40000
	s_addc_u32 s71, s71, 0
	s_mov_b32 m0, s16
	v_lshl_add_u64 v[216:217], s[70:71], 0, v[144:145]
	ds_read_b128 v[178:181], v222 offset:32768
	ds_read_b128 v[182:185], v222 offset:33792
	ds_read_b128 v[186:189], v222 offset:34816
	ds_read_b128 v[190:193], v222 offset:35840
	ds_read_b128 v[194:197], v222 offset:36864
	ds_read_b128 v[198:201], v222 offset:37888
	ds_read_b128 v[202:205], v222 offset:38912
	ds_read_b128 v[206:209], v222 offset:39936
	global_load_lds_dwordx4 v[216:217], off
	v_lshl_add_u64 v[216:217], s[70:71], 0, v[146:147]
	s_mov_b32 m0, s20
	s_nop 0
	global_load_lds_dwordx4 v[216:217], off
	s_waitcnt vmcnt(8)
	s_waitcnt lgkmcnt(0)
	s_barrier
	s_setprio 1
	s_waitcnt lgkmcnt(0)
	v_mfma_f32_16x16x32_bf16 v[138:141], v[106:109], v[178:181], v[138:141]
	v_mfma_f32_16x16x32_bf16 v[62:65], v[114:117], v[178:181], v[62:65]
	v_mfma_f32_16x16x32_bf16 v[130:133], v[106:109], v[186:189], v[130:133]
	v_mfma_f32_16x16x32_bf16 v[54:57], v[114:117], v[186:189], v[54:57]
	v_mfma_f32_16x16x32_bf16 v[122:125], v[106:109], v[194:197], v[122:125]
	v_mfma_f32_16x16x32_bf16 v[46:49], v[114:117], v[194:197], v[46:49]
	v_mfma_f32_16x16x32_bf16 v[102:105], v[106:109], v[202:205], v[102:105]
	v_mfma_f32_16x16x32_bf16 v[38:41], v[114:117], v[202:205], v[38:41]
	v_mfma_f32_16x16x32_bf16 v[138:141], v[110:113], v[182:185], v[138:141]
	v_mfma_f32_16x16x32_bf16 v[62:65], v[152:155], v[182:185], v[62:65]
	v_mfma_f32_16x16x32_bf16 v[130:133], v[110:113], v[190:193], v[130:133]
	v_mfma_f32_16x16x32_bf16 v[54:57], v[152:155], v[190:193], v[54:57]
	v_mfma_f32_16x16x32_bf16 v[122:125], v[110:113], v[198:201], v[122:125]
	v_mfma_f32_16x16x32_bf16 v[46:49], v[152:155], v[198:201], v[46:49]
	v_mfma_f32_16x16x32_bf16 v[102:105], v[110:113], v[206:209], v[102:105]
	v_mfma_f32_16x16x32_bf16 v[38:41], v[152:155], v[206:209], v[38:41]
	s_setprio 0
	s_setprio 1
	v_mfma_f32_16x16x32_bf16 v[134:137], v[156:159], v[178:181], v[134:137]
	v_mfma_f32_16x16x32_bf16 v[58:61], v[170:173], v[178:181], v[58:61]
	v_mfma_f32_16x16x32_bf16 v[126:129], v[156:159], v[186:189], v[126:129]
	v_mfma_f32_16x16x32_bf16 v[50:53], v[170:173], v[186:189], v[50:53]
	v_mfma_f32_16x16x32_bf16 v[118:121], v[156:159], v[194:197], v[118:121]
	v_mfma_f32_16x16x32_bf16 v[42:45], v[170:173], v[194:197], v[42:45]
	v_mfma_f32_16x16x32_bf16 v[98:101], v[156:159], v[202:205], v[98:101]
	v_mfma_f32_16x16x32_bf16 v[34:37], v[170:173], v[202:205], v[34:37]
	v_mfma_f32_16x16x32_bf16 v[134:137], v[160:163], v[182:185], v[134:137]
	v_mfma_f32_16x16x32_bf16 v[58:61], v[174:177], v[182:185], v[58:61]
	v_mfma_f32_16x16x32_bf16 v[126:129], v[160:163], v[190:193], v[126:129]
	v_mfma_f32_16x16x32_bf16 v[50:53], v[174:177], v[190:193], v[50:53]
	v_mfma_f32_16x16x32_bf16 v[118:121], v[160:163], v[198:201], v[118:121]
	v_mfma_f32_16x16x32_bf16 v[42:45], v[174:177], v[198:201], v[42:45]
	v_mfma_f32_16x16x32_bf16 v[98:101], v[160:163], v[206:209], v[98:101]
	v_mfma_f32_16x16x32_bf16 v[34:37], v[174:177], v[206:209], v[34:37]
	s_setprio 0
	s_barrier
	s_add_i32 s70, s74, s13
	v_lshl_add_u64 v[164:165], v[164:165], 0, s[56:57]
	s_mov_b32 m0, s70
	ds_read_b128 v[178:181], v222 offset:49152
	ds_read_b128 v[182:185], v222 offset:50176
	ds_read_b128 v[186:189], v222 offset:51200
	ds_read_b128 v[190:193], v222 offset:52224
	ds_read_b128 v[194:197], v222 offset:53248
	ds_read_b128 v[198:201], v222 offset:54272
	ds_read_b128 v[202:205], v222 offset:55296
	ds_read_b128 v[206:209], v222 offset:56320
	global_load_lds_dwordx4 v[164:165], off
	s_add_i32 m0, s70, 0x2000
	s_add_u32 s68, s68, 0x8080
	v_lshl_add_u64 v[164:165], v[210:211], 0, s[56:57]
	s_addc_u32 s69, s69, 0
	s_add_i32 s70, s75, s13
	global_load_lds_dwordx4 v[164:165], off
	v_lshl_add_u64 v[164:165], s[68:69], 0, v[166:167]
	s_mov_b32 m0, s70
	s_nop 0
	global_load_lds_dwordx4 v[164:165], off
	v_lshl_add_u64 v[164:165], s[68:69], 0, v[142:143]
	s_add_i32 m0, s70, 0x2000
	s_nop 0
	global_load_lds_dwordx4 v[164:165], off
	v_lshl_add_u64 v[164:165], v[212:213], 0, s[56:57]
	s_mov_b32 m0, s21
	s_nop 0
	global_load_lds_dwordx4 v[164:165], off
	v_lshl_add_u64 v[164:165], v[214:215], 0, s[56:57]
	s_mov_b32 m0, s22
	s_nop 0
	global_load_lds_dwordx4 v[164:165], off
	s_waitcnt vmcnt(8)
	s_waitcnt lgkmcnt(0)
	s_barrier
	s_setprio 1
	s_waitcnt lgkmcnt(0)
	v_mfma_f32_16x16x32_bf16 v[94:97], v[106:109], v[178:181], v[94:97]
	v_mfma_f32_16x16x32_bf16 v[30:33], v[114:117], v[178:181], v[30:33]
	v_mfma_f32_16x16x32_bf16 v[86:89], v[106:109], v[186:189], v[86:89]
	v_mfma_f32_16x16x32_bf16 v[22:25], v[114:117], v[186:189], v[22:25]
	v_mfma_f32_16x16x32_bf16 v[78:81], v[106:109], v[194:197], v[78:81]
	v_mfma_f32_16x16x32_bf16 v[14:17], v[114:117], v[194:197], v[14:17]
	v_mfma_f32_16x16x32_bf16 v[70:73], v[106:109], v[202:205], v[70:73]
	v_mfma_f32_16x16x32_bf16 v[6:9], v[114:117], v[202:205], v[6:9]
	v_mfma_f32_16x16x32_bf16 v[94:97], v[110:113], v[182:185], v[94:97]
	v_mfma_f32_16x16x32_bf16 v[30:33], v[152:155], v[182:185], v[30:33]
	v_mfma_f32_16x16x32_bf16 v[86:89], v[110:113], v[190:193], v[86:89]
	v_mfma_f32_16x16x32_bf16 v[22:25], v[152:155], v[190:193], v[22:25]
	v_mfma_f32_16x16x32_bf16 v[78:81], v[110:113], v[198:201], v[78:81]
	v_mfma_f32_16x16x32_bf16 v[14:17], v[152:155], v[198:201], v[14:17]
	v_mfma_f32_16x16x32_bf16 v[70:73], v[110:113], v[206:209], v[70:73]
	v_mfma_f32_16x16x32_bf16 v[6:9], v[152:155], v[206:209], v[6:9]
	s_setprio 0
	s_setprio 1
	v_mfma_f32_16x16x32_bf16 v[90:93], v[156:159], v[178:181], v[90:93]
	v_mfma_f32_16x16x32_bf16 v[26:29], v[170:173], v[178:181], v[26:29]
	v_mfma_f32_16x16x32_bf16 v[82:85], v[156:159], v[186:189], v[82:85]
	v_mfma_f32_16x16x32_bf16 v[18:21], v[170:173], v[186:189], v[18:21]
	v_mfma_f32_16x16x32_bf16 v[74:77], v[156:159], v[194:197], v[74:77]
	v_mfma_f32_16x16x32_bf16 v[10:13], v[170:173], v[194:197], v[10:13]
	v_mfma_f32_16x16x32_bf16 v[66:69], v[156:159], v[202:205], v[66:69]
	v_mfma_f32_16x16x32_bf16 v[2:5], v[170:173], v[202:205], v[2:5]
	v_mfma_f32_16x16x32_bf16 v[90:93], v[160:163], v[182:185], v[90:93]
	v_mfma_f32_16x16x32_bf16 v[26:29], v[174:177], v[182:185], v[26:29]
	v_mfma_f32_16x16x32_bf16 v[82:85], v[160:163], v[190:193], v[82:85]
	v_mfma_f32_16x16x32_bf16 v[18:21], v[174:177], v[190:193], v[18:21]
	v_mfma_f32_16x16x32_bf16 v[74:77], v[160:163], v[198:201], v[74:77]
	v_mfma_f32_16x16x32_bf16 v[10:13], v[174:177], v[198:201], v[10:13]
	v_mfma_f32_16x16x32_bf16 v[66:69], v[160:163], v[206:209], v[66:69]
	v_mfma_f32_16x16x32_bf16 v[2:5], v[174:177], v[206:209], v[2:5]
	s_setprio 0
	s_add_u32 s66, s66, 0x100
	s_addc_u32 s72, s72, 0
	s_add_u32 s64, s64, 0x100
	s_addc_u32 s65, s65, 0
	s_cmp_ge_i32 s73, s1
	s_mov_b32 s68, s73
	s_cbranch_scc1 .Lq4skip_ph3
	s_barrier
	s_branch .LBB0_469
.Lq4skip_ph3:
	s_nop 1
	s_branch .LBB0_471

.LBB0_817:
	s_add_i32 s69, s58, 2
	s_add_u32 s59, s54, 0xfffc0080
	s_addc_u32 s60, s55, -1
	s_add_i32 s70, 0, 0x10000
	s_cmp_eq_u32 s53, s58
	s_cselect_b32 s61, s43, s60
	s_cselect_b32 s60, s45, s59
	v_add_u32_e32 v146, s70, v151
	s_cselect_b32 s59, s64, s68
	s_cselect_b32 s58, s65, s66
	s_add_i32 s72, 0, 0x14000
	ds_read_b128 v[142:145], v146
	ds_read_b128 v[156:159], v146 offset:1024
	ds_read_b128 v[160:163], v146 offset:2048
	ds_read_b128 v[170:173], v146 offset:3072
	v_add_u32_e32 v146, s72, v151
	ds_read_b128 v[174:177], v146
	ds_read_b128 v[178:181], v146 offset:1024
	ds_read_b128 v[182:185], v146 offset:2048
	ds_read_b128 v[186:189], v146 offset:3072
	v_lshl_add_u64 v[146:147], s[54:55], 0, v[140:141]
	s_add_i32 m0, s16, 0xc000
	ds_read_b128 v[190:193], v154
	ds_read_b128 v[194:197], v154 offset:1024
	ds_read_b128 v[198:201], v154 offset:2048
	ds_read_b128 v[202:205], v154 offset:3072
	ds_read_b128 v[206:209], v154 offset:4096
	ds_read_b128 v[210:213], v154 offset:5120
	ds_read_b128 v[214:217], v154 offset:6144
	ds_read_b128 v[218:221], v154 offset:7168
	global_load_lds_dwordx4 v[146:147], off
	v_lshl_add_u64 v[146:147], s[54:55], 0, v[138:139]
	s_add_i32 m0, s16, 0xe000
	s_nop 0
	global_load_lds_dwordx4 v[146:147], off
	s_waitcnt vmcnt(8)
	s_waitcnt lgkmcnt(0)
	s_barrier
	s_setprio 1
	s_waitcnt lgkmcnt(0)
	v_mfma_f32_16x16x32_bf16 v[126:129], v[142:145], v[190:193], v[126:129]
	v_mfma_f32_16x16x32_bf16 v[118:121], v[160:163], v[190:193], v[118:121]
	v_mfma_f32_16x16x32_bf16 v[110:113], v[142:145], v[198:201], v[110:113]
	v_mfma_f32_16x16x32_bf16 v[102:105], v[160:163], v[198:201], v[102:105]
	v_mfma_f32_16x16x32_bf16 v[94:97], v[142:145], v[206:209], v[94:97]
	v_mfma_f32_16x16x32_bf16 v[86:89], v[160:163], v[206:209], v[86:89]
	v_mfma_f32_16x16x32_bf16 v[78:81], v[142:145], v[214:217], v[78:81]
	v_mfma_f32_16x16x32_bf16 v[70:73], v[160:163], v[214:217], v[70:73]
	v_mfma_f32_16x16x32_bf16 v[126:129], v[156:159], v[194:197], v[126:129]
	v_mfma_f32_16x16x32_bf16 v[118:121], v[170:173], v[194:197], v[118:121]
	v_mfma_f32_16x16x32_bf16 v[110:113], v[156:159], v[202:205], v[110:113]
	v_mfma_f32_16x16x32_bf16 v[102:105], v[170:173], v[202:205], v[102:105]
	v_mfma_f32_16x16x32_bf16 v[94:97], v[156:159], v[210:213], v[94:97]
	v_mfma_f32_16x16x32_bf16 v[86:89], v[170:173], v[210:213], v[86:89]
	v_mfma_f32_16x16x32_bf16 v[78:81], v[156:159], v[218:221], v[78:81]
	v_mfma_f32_16x16x32_bf16 v[70:73], v[170:173], v[218:221], v[70:73]
	s_setprio 0
	s_setprio 1
	v_mfma_f32_16x16x32_bf16 v[122:125], v[174:177], v[190:193], v[122:125]
	v_mfma_f32_16x16x32_bf16 v[114:117], v[182:185], v[190:193], v[114:117]
	v_mfma_f32_16x16x32_bf16 v[106:109], v[174:177], v[198:201], v[106:109]
	v_mfma_f32_16x16x32_bf16 v[98:101], v[182:185], v[198:201], v[98:101]
	v_mfma_f32_16x16x32_bf16 v[90:93], v[174:177], v[206:209], v[90:93]
	v_mfma_f32_16x16x32_bf16 v[82:85], v[182:185], v[206:209], v[82:85]
	v_mfma_f32_16x16x32_bf16 v[74:77], v[174:177], v[214:217], v[74:77]
	v_mfma_f32_16x16x32_bf16 v[66:69], v[182:185], v[214:217], v[66:69]
	v_mfma_f32_16x16x32_bf16 v[122:125], v[178:181], v[194:197], v[122:125]
	v_mfma_f32_16x16x32_bf16 v[114:117], v[186:189], v[194:197], v[114:117]
	v_mfma_f32_16x16x32_bf16 v[106:109], v[178:181], v[202:205], v[106:109]
	v_mfma_f32_16x16x32_bf16 v[98:101], v[186:189], v[202:205], v[98:101]
	v_mfma_f32_16x16x32_bf16 v[90:93], v[178:181], v[210:213], v[90:93]
	v_mfma_f32_16x16x32_bf16 v[82:85], v[186:189], v[210:213], v[82:85]
	v_mfma_f32_16x16x32_bf16 v[74:77], v[178:181], v[218:221], v[74:77]
	v_mfma_f32_16x16x32_bf16 v[66:69], v[186:189], v[218:221], v[66:69]
	s_setprio 0
	s_barrier
	s_add_i32 s70, s70, s14
	v_lshl_add_u64 v[146:147], s[58:59], 0, v[166:167]
	s_mov_b32 m0, s70
	ds_read_b128 v[190:193], v154 offset:16384
	ds_read_b128 v[194:197], v154 offset:17408
	ds_read_b128 v[198:201], v154 offset:18432
	ds_read_b128 v[202:205], v154 offset:19456
	ds_read_b128 v[206:209], v154 offset:20480
	ds_read_b128 v[210:213], v154 offset:21504
	ds_read_b128 v[214:217], v154 offset:22528
	ds_read_b128 v[218:221], v154 offset:23552
	global_load_lds_dwordx4 v[146:147], off
	s_add_i32 m0, s70, 0x2000
	s_add_u32 s70, s58, 0x40000
	v_lshl_add_u64 v[164:165], s[58:59], 0, v[134:135]
	s_addc_u32 s71, s59, 0
	s_add_i32 s72, s72, s14
	global_load_lds_dwordx4 v[164:165], off
	v_lshl_add_u64 v[222:223], s[70:71], 0, v[166:167]
	s_mov_b32 m0, s72
	v_lshl_add_u64 v[232:233], s[60:61], 0, v[130:131]
	global_load_lds_dwordx4 v[222:223], off
	v_lshl_add_u64 v[222:223], s[70:71], 0, v[134:135]
	s_add_i32 m0, s72, 0x2000
	s_nop 0
	global_load_lds_dwordx4 v[222:223], off
	v_lshl_add_u64 v[222:223], s[60:61], 0, v[132:133]
	s_mov_b32 m0, s16
	s_nop 0
	global_load_lds_dwordx4 v[222:223], off
	s_mov_b32 m0, s20
	s_nop 0
	global_load_lds_dwordx4 v[232:233], off
	s_waitcnt vmcnt(8)
	s_waitcnt lgkmcnt(0)
	s_barrier
	s_setprio 1
	s_waitcnt lgkmcnt(0)
	v_mfma_f32_16x16x32_bf16 v[62:65], v[142:145], v[190:193], v[62:65]
	v_mfma_f32_16x16x32_bf16 v[54:57], v[160:163], v[190:193], v[54:57]
	v_mfma_f32_16x16x32_bf16 v[46:49], v[142:145], v[198:201], v[46:49]
	v_mfma_f32_16x16x32_bf16 v[38:41], v[160:163], v[198:201], v[38:41]
	v_mfma_f32_16x16x32_bf16 v[30:33], v[142:145], v[206:209], v[30:33]
	v_mfma_f32_16x16x32_bf16 v[22:25], v[160:163], v[206:209], v[22:25]
	v_mfma_f32_16x16x32_bf16 v[14:17], v[142:145], v[214:217], v[14:17]
	v_mfma_f32_16x16x32_bf16 v[6:9], v[160:163], v[214:217], v[6:9]
	v_mfma_f32_16x16x32_bf16 v[62:65], v[156:159], v[194:197], v[62:65]
	v_mfma_f32_16x16x32_bf16 v[54:57], v[170:173], v[194:197], v[54:57]
	v_mfma_f32_16x16x32_bf16 v[46:49], v[156:159], v[202:205], v[46:49]
	v_mfma_f32_16x16x32_bf16 v[38:41], v[170:173], v[202:205], v[38:41]
	v_mfma_f32_16x16x32_bf16 v[30:33], v[156:159], v[210:213], v[30:33]
	v_mfma_f32_16x16x32_bf16 v[22:25], v[170:173], v[210:213], v[22:25]
	v_mfma_f32_16x16x32_bf16 v[14:17], v[156:159], v[218:221], v[14:17]
	v_mfma_f32_16x16x32_bf16 v[6:9], v[170:173], v[218:221], v[6:9]
	s_setprio 0
	s_setprio 1
	v_mfma_f32_16x16x32_bf16 v[58:61], v[174:177], v[190:193], v[58:61]
	v_mfma_f32_16x16x32_bf16 v[50:53], v[182:185], v[190:193], v[50:53]
	v_mfma_f32_16x16x32_bf16 v[42:45], v[174:177], v[198:201], v[42:45]
	v_mfma_f32_16x16x32_bf16 v[34:37], v[182:185], v[198:201], v[34:37]
	v_mfma_f32_16x16x32_bf16 v[26:29], v[174:177], v[206:209], v[26:29]
	v_mfma_f32_16x16x32_bf16 v[18:21], v[182:185], v[206:209], v[18:21]
	v_mfma_f32_16x16x32_bf16 v[10:13], v[174:177], v[214:217], v[10:13]
	v_mfma_f32_16x16x32_bf16 v[2:5], v[182:185], v[214:217], v[2:5]
	v_mfma_f32_16x16x32_bf16 v[58:61], v[178:181], v[194:197], v[58:61]
	v_mfma_f32_16x16x32_bf16 v[50:53], v[186:189], v[194:197], v[50:53]
	v_mfma_f32_16x16x32_bf16 v[42:45], v[178:181], v[202:205], v[42:45]
	v_mfma_f32_16x16x32_bf16 v[34:37], v[186:189], v[202:205], v[34:37]
	v_mfma_f32_16x16x32_bf16 v[26:29], v[178:181], v[210:213], v[26:29]
	v_mfma_f32_16x16x32_bf16 v[18:21], v[186:189], v[210:213], v[18:21]
	v_mfma_f32_16x16x32_bf16 v[10:13], v[178:181], v[218:221], v[10:13]
	v_mfma_f32_16x16x32_bf16 v[2:5], v[186:189], v[218:221], v[2:5]
	s_setprio 0
	s_barrier
	s_add_i32 s70, 0, 0x18000
	v_add_u32_e32 v148, s70, v151
	s_add_i32 s71, 0, 0x1c000
	ds_read_b128 v[142:145], v148
	ds_read_b128 v[156:159], v148 offset:1024
	ds_read_b128 v[160:163], v148 offset:2048
	ds_read_b128 v[170:173], v148 offset:3072
	v_add_u32_e32 v148, s71, v151
	ds_read_b128 v[174:177], v148
	ds_read_b128 v[178:181], v148 offset:1024
	ds_read_b128 v[182:185], v148 offset:2048
	ds_read_b128 v[186:189], v148 offset:3072
	s_add_u32 s60, s60, 0x40000
	s_addc_u32 s61, s61, 0
	s_mov_b32 m0, s21
	v_lshl_add_u64 v[234:235], s[60:61], 0, v[132:133]
	ds_read_b128 v[190:193], v154 offset:32768
	ds_read_b128 v[194:197], v154 offset:33792
	ds_read_b128 v[198:201], v154 offset:34816
	ds_read_b128 v[202:205], v154 offset:35840
	ds_read_b128 v[206:209], v154 offset:36864
	ds_read_b128 v[210:213], v154 offset:37888
	ds_read_b128 v[214:217], v154 offset:38912
	ds_read_b128 v[218:221], v154 offset:39936
	global_load_lds_dwordx4 v[234:235], off
	v_lshl_add_u64 v[234:235], s[60:61], 0, v[130:131]
	s_mov_b32 m0, s22
	s_nop 0
	global_load_lds_dwordx4 v[234:235], off
	s_waitcnt vmcnt(8)
	s_waitcnt lgkmcnt(0)
	s_barrier
	s_setprio 1
	s_waitcnt lgkmcnt(0)
	v_mfma_f32_16x16x32_bf16 v[126:129], v[142:145], v[190:193], v[126:129]
	v_mfma_f32_16x16x32_bf16 v[118:121], v[160:163], v[190:193], v[118:121]
	v_mfma_f32_16x16x32_bf16 v[110:113], v[142:145], v[198:201], v[110:113]
	v_mfma_f32_16x16x32_bf16 v[102:105], v[160:163], v[198:201], v[102:105]
	v_mfma_f32_16x16x32_bf16 v[94:97], v[142:145], v[206:209], v[94:97]
	v_mfma_f32_16x16x32_bf16 v[86:89], v[160:163], v[206:209], v[86:89]
	v_mfma_f32_16x16x32_bf16 v[78:81], v[142:145], v[214:217], v[78:81]
	v_mfma_f32_16x16x32_bf16 v[70:73], v[160:163], v[214:217], v[70:73]
	v_mfma_f32_16x16x32_bf16 v[126:129], v[156:159], v[194:197], v[126:129]
	v_mfma_f32_16x16x32_bf16 v[118:121], v[170:173], v[194:197], v[118:121]
	v_mfma_f32_16x16x32_bf16 v[110:113], v[156:159], v[202:205], v[110:113]
	v_mfma_f32_16x16x32_bf16 v[102:105], v[170:173], v[202:205], v[102:105]
	v_mfma_f32_16x16x32_bf16 v[94:97], v[156:159], v[210:213], v[94:97]
	v_mfma_f32_16x16x32_bf16 v[86:89], v[170:173], v[210:213], v[86:89]
	v_mfma_f32_16x16x32_bf16 v[78:81], v[156:159], v[218:221], v[78:81]
	v_mfma_f32_16x16x32_bf16 v[70:73], v[170:173], v[218:221], v[70:73]
	s_setprio 0
	s_setprio 1
	v_mfma_f32_16x16x32_bf16 v[122:125], v[174:177], v[190:193], v[122:125]
	v_mfma_f32_16x16x32_bf16 v[114:117], v[182:185], v[190:193], v[114:117]
	v_mfma_f32_16x16x32_bf16 v[106:109], v[174:177], v[198:201], v[106:109]
	v_mfma_f32_16x16x32_bf16 v[98:101], v[182:185], v[198:201], v[98:101]
	v_mfma_f32_16x16x32_bf16 v[90:93], v[174:177], v[206:209], v[90:93]
	v_mfma_f32_16x16x32_bf16 v[82:85], v[182:185], v[206:209], v[82:85]
	v_mfma_f32_16x16x32_bf16 v[74:77], v[174:177], v[214:217], v[74:77]
	v_mfma_f32_16x16x32_bf16 v[66:69], v[182:185], v[214:217], v[66:69]
	v_mfma_f32_16x16x32_bf16 v[122:125], v[178:181], v[194:197], v[122:125]
	v_mfma_f32_16x16x32_bf16 v[114:117], v[186:189], v[194:197], v[114:117]
	v_mfma_f32_16x16x32_bf16 v[106:109], v[178:181], v[202:205], v[106:109]
	v_mfma_f32_16x16x32_bf16 v[98:101], v[186:189], v[202:205], v[98:101]
	v_mfma_f32_16x16x32_bf16 v[90:93], v[178:181], v[210:213], v[90:93]
	v_mfma_f32_16x16x32_bf16 v[82:85], v[186:189], v[210:213], v[82:85]
	v_mfma_f32_16x16x32_bf16 v[74:77], v[178:181], v[218:221], v[74:77]
	v_mfma_f32_16x16x32_bf16 v[66:69], v[186:189], v[218:221], v[66:69]
	s_setprio 0
	s_barrier
	s_add_i32 s60, s70, s14
	v_lshl_add_u64 v[146:147], v[146:147], 0, s[56:57]
	s_mov_b32 m0, s60
	ds_read_b128 v[190:193], v154 offset:49152
	ds_read_b128 v[194:197], v154 offset:50176
	ds_read_b128 v[198:201], v154 offset:51200
	ds_read_b128 v[202:205], v154 offset:52224
	ds_read_b128 v[206:209], v154 offset:53248
	ds_read_b128 v[210:213], v154 offset:54272
	ds_read_b128 v[214:217], v154 offset:55296
	ds_read_b128 v[218:221], v154 offset:56320
	global_load_lds_dwordx4 v[146:147], off
	s_add_i32 m0, s60, 0x2000
	s_add_u32 s58, s58, 0x40080
	v_lshl_add_u64 v[146:147], v[164:165], 0, s[56:57]
	s_addc_u32 s59, s59, 0
	s_add_i32 s60, s71, s14
	global_load_lds_dwordx4 v[146:147], off
	v_lshl_add_u64 v[146:147], s[58:59], 0, v[166:167]
	s_mov_b32 m0, s60
	s_nop 0
	global_load_lds_dwordx4 v[146:147], off
	v_lshl_add_u64 v[146:147], s[58:59], 0, v[134:135]
	s_add_i32 m0, s60, 0x2000
	s_nop 0
	global_load_lds_dwordx4 v[146:147], off
	v_lshl_add_u64 v[146:147], v[222:223], 0, s[56:57]
	s_mov_b32 m0, s23
	s_nop 0
	global_load_lds_dwordx4 v[146:147], off
	v_lshl_add_u64 v[146:147], v[232:233], 0, s[56:57]
	s_mov_b32 m0, s24
	s_nop 0
	global_load_lds_dwordx4 v[146:147], off
	s_waitcnt vmcnt(8)
	s_waitcnt lgkmcnt(0)
	s_barrier
	s_setprio 1
	s_waitcnt lgkmcnt(0)
	v_mfma_f32_16x16x32_bf16 v[62:65], v[142:145], v[190:193], v[62:65]
	v_mfma_f32_16x16x32_bf16 v[54:57], v[160:163], v[190:193], v[54:57]
	v_mfma_f32_16x16x32_bf16 v[46:49], v[142:145], v[198:201], v[46:49]
	v_mfma_f32_16x16x32_bf16 v[38:41], v[160:163], v[198:201], v[38:41]
	v_mfma_f32_16x16x32_bf16 v[30:33], v[142:145], v[206:209], v[30:33]
	v_mfma_f32_16x16x32_bf16 v[22:25], v[160:163], v[206:209], v[22:25]
	v_mfma_f32_16x16x32_bf16 v[14:17], v[142:145], v[214:217], v[14:17]
	v_mfma_f32_16x16x32_bf16 v[6:9], v[160:163], v[214:217], v[6:9]
	v_mfma_f32_16x16x32_bf16 v[62:65], v[156:159], v[194:197], v[62:65]
	v_mfma_f32_16x16x32_bf16 v[54:57], v[170:173], v[194:197], v[54:57]
	v_mfma_f32_16x16x32_bf16 v[46:49], v[156:159], v[202:205], v[46:49]
	v_mfma_f32_16x16x32_bf16 v[38:41], v[170:173], v[202:205], v[38:41]
	v_mfma_f32_16x16x32_bf16 v[30:33], v[156:159], v[210:213], v[30:33]
	v_mfma_f32_16x16x32_bf16 v[22:25], v[170:173], v[210:213], v[22:25]
	v_mfma_f32_16x16x32_bf16 v[14:17], v[156:159], v[218:221], v[14:17]
	v_mfma_f32_16x16x32_bf16 v[6:9], v[170:173], v[218:221], v[6:9]
	s_setprio 0
	s_setprio 1
	v_mfma_f32_16x16x32_bf16 v[58:61], v[174:177], v[190:193], v[58:61]
	v_mfma_f32_16x16x32_bf16 v[50:53], v[182:185], v[190:193], v[50:53]
	v_mfma_f32_16x16x32_bf16 v[42:45], v[174:177], v[198:201], v[42:45]
	v_mfma_f32_16x16x32_bf16 v[34:37], v[182:185], v[198:201], v[34:37]
	v_mfma_f32_16x16x32_bf16 v[26:29], v[174:177], v[206:209], v[26:29]
	v_mfma_f32_16x16x32_bf16 v[18:21], v[182:185], v[206:209], v[18:21]
	v_mfma_f32_16x16x32_bf16 v[10:13], v[174:177], v[214:217], v[10:13]
	v_mfma_f32_16x16x32_bf16 v[2:5], v[182:185], v[214:217], v[2:5]
	v_mfma_f32_16x16x32_bf16 v[58:61], v[178:181], v[194:197], v[58:61]
	v_mfma_f32_16x16x32_bf16 v[50:53], v[186:189], v[194:197], v[50:53]
	v_mfma_f32_16x16x32_bf16 v[42:45], v[178:181], v[202:205], v[42:45]
	v_mfma_f32_16x16x32_bf16 v[34:37], v[186:189], v[202:205], v[34:37]
	v_mfma_f32_16x16x32_bf16 v[26:29], v[178:181], v[210:213], v[26:29]
	v_mfma_f32_16x16x32_bf16 v[18:21], v[186:189], v[210:213], v[18:21]
	v_mfma_f32_16x16x32_bf16 v[10:13], v[178:181], v[218:221], v[10:13]
	v_mfma_f32_16x16x32_bf16 v[2:5], v[186:189], v[218:221], v[2:5]
	s_setprio 0
	s_add_u32 s66, s66, 0x100
	s_addc_u32 s68, s68, 0
	s_add_u32 s54, s54, 0x100
	s_addc_u32 s55, s55, 0
	s_cmp_ge_i32 s69, s13
	s_mov_b32 s58, s69
	s_cbranch_scc1 .Lq4skip_ph7b
	s_barrier
	s_branch .LBB0_817
.Lq4skip_ph7b:
	s_nop 1
	s_mov_b64 s[72:73], 0xe800000
	s_mov_b64 s[70:71], 0xe800800
	v_mov_b32_e32 v209, v1
	s_and_b64 vcc, exec, s[36:37]
	s_cbranch_vccz .LBB0_820

.LBB0_842:
	s_add_i32 s66, s54, 2
	s_add_u32 s55, s52, 0xfffe0080
	s_addc_u32 s58, s53, -1
	s_add_i32 s68, 0, 0x10000
	s_cmp_eq_u32 s51, s54
	s_cselect_b32 s59, s41, s58
	s_cselect_b32 s58, s43, s55
	s_cselect_b32 s55, s62, s65
	s_cselect_b32 s54, s63, s64
	s_add_i32 s69, 0, 0x14000
	v_add_u32_e32 v2, s68, v196
	v_add_u32_e32 v6, s69, v196
	ds_read_b128 v[26:29], v2
	ds_read_b128 v[30:33], v2 offset:1024
	ds_read_b128 v[18:21], v2 offset:2048
	ds_read_b128 v[22:25], v2 offset:3072
	ds_read_b128 v[10:13], v6
	ds_read_b128 v[14:17], v6 offset:1024
	ds_read_b128 v[2:5], v6 offset:2048
	ds_read_b128 v[6:9], v6 offset:3072
	v_lshl_add_u64 v[170:171], s[52:53], 0, v[184:185]
	s_add_i32 m0, s16, 0xc000
	ds_read_b128 v[186:189], v198
	ds_read_b128 v[190:193], v198 offset:1024
	ds_read_b128 v[200:203], v198 offset:2048
	ds_read_b128 v[204:207], v198 offset:3072
	ds_read_b128 v[208:211], v198 offset:4096
	ds_read_b128 v[212:215], v198 offset:5120
	ds_read_b128 v[216:219], v198 offset:6144
	ds_read_b128 v[220:223], v198 offset:7168
	global_load_lds_dwordx4 v[170:171], off
	v_lshl_add_u64 v[170:171], s[52:53], 0, v[182:183]
	s_add_i32 m0, s16, 0xe000
	s_nop 0
	global_load_lds_dwordx4 v[170:171], off
	s_waitcnt vmcnt(8)
	s_waitcnt lgkmcnt(0)
	s_barrier
	s_setprio 1
	s_waitcnt lgkmcnt(0)
	v_mfma_scale_f32_16x16x128_f8f6f4 v[158:161], v[26:33], v[186:193], v[158:161], v194, v169 op_sel_hi:[0,0,0]
	v_mfma_scale_f32_16x16x128_f8f6f4 v[150:153], v[18:25], v[186:193], v[150:153], v194, v169 op_sel_hi:[0,0,0]
	v_mfma_scale_f32_16x16x128_f8f6f4 v[142:145], v[26:33], v[200:207], v[142:145], v194, v169 op_sel_hi:[0,0,0]
	v_mfma_scale_f32_16x16x128_f8f6f4 v[134:137], v[18:25], v[200:207], v[134:137], v194, v169 op_sel_hi:[0,0,0]
	v_mfma_scale_f32_16x16x128_f8f6f4 v[126:129], v[26:33], v[208:215], v[126:129], v194, v169 op_sel_hi:[0,0,0]
	v_mfma_scale_f32_16x16x128_f8f6f4 v[118:121], v[18:25], v[208:215], v[118:121], v194, v169 op_sel_hi:[0,0,0]
	v_mfma_scale_f32_16x16x128_f8f6f4 v[110:113], v[26:33], v[216:223], v[110:113], v194, v169 op_sel_hi:[0,0,0]
	v_mfma_scale_f32_16x16x128_f8f6f4 v[102:105], v[18:25], v[216:223], v[102:105], v194, v169 op_sel_hi:[0,0,0]
	s_setprio 0
	s_setprio 1
	v_mfma_scale_f32_16x16x128_f8f6f4 v[154:157], v[10:17], v[186:193], v[154:157], v194, v169 op_sel_hi:[0,0,0]
	v_mfma_scale_f32_16x16x128_f8f6f4 v[146:149], v[2:9], v[186:193], v[146:149], v194, v169 op_sel_hi:[0,0,0]
	v_mfma_scale_f32_16x16x128_f8f6f4 v[138:141], v[10:17], v[200:207], v[138:141], v194, v169 op_sel_hi:[0,0,0]
	v_mfma_scale_f32_16x16x128_f8f6f4 v[130:133], v[2:9], v[200:207], v[130:133], v194, v169 op_sel_hi:[0,0,0]
	v_mfma_scale_f32_16x16x128_f8f6f4 v[122:125], v[10:17], v[208:215], v[122:125], v194, v169 op_sel_hi:[0,0,0]
	v_mfma_scale_f32_16x16x128_f8f6f4 v[114:117], v[2:9], v[208:215], v[114:117], v194, v169 op_sel_hi:[0,0,0]
	v_mfma_scale_f32_16x16x128_f8f6f4 v[106:109], v[10:17], v[216:223], v[106:109], v194, v169 op_sel_hi:[0,0,0]
	v_mfma_scale_f32_16x16x128_f8f6f4 v[98:101], v[2:9], v[216:223], v[98:101], v194, v169 op_sel_hi:[0,0,0]
	s_setprio 0
	s_barrier
	s_add_i32 s68, s68, s14
	v_lshl_add_u64 v[186:187], s[54:55], 0, v[166:167]
	s_mov_b32 m0, s68
	ds_read_b128 v[200:203], v198 offset:16384
	ds_read_b128 v[204:207], v198 offset:17408
	ds_read_b128 v[208:211], v198 offset:18432
	ds_read_b128 v[212:215], v198 offset:19456
	ds_read_b128 v[216:219], v198 offset:20480
	ds_read_b128 v[220:223], v198 offset:21504
	ds_read_b128 v[236:239], v198 offset:22528
	ds_read_b128 v[240:243], v198 offset:23552
	global_load_lds_dwordx4 v[186:187], off
	s_add_i32 m0, s68, 0x2000
	s_add_u32 s70, s54, 0x20000
	v_lshl_add_u64 v[188:189], s[54:55], 0, v[178:179]
	s_addc_u32 s71, s55, 0
	s_add_i32 s68, s69, s14
	global_load_lds_dwordx4 v[188:189], off
	v_lshl_add_u64 v[170:171], s[70:71], 0, v[166:167]
	s_mov_b32 m0, s68
	v_lshl_add_u64 v[190:191], s[58:59], 0, v[164:165]
	global_load_lds_dwordx4 v[170:171], off
	v_lshl_add_u64 v[170:171], s[70:71], 0, v[178:179]
	s_add_i32 m0, s68, 0x2000
	v_lshl_add_u64 v[192:193], s[58:59], 0, v[162:163]
	global_load_lds_dwordx4 v[170:171], off
	s_mov_b32 m0, s16
	s_nop 0
	global_load_lds_dwordx4 v[190:191], off
	s_mov_b32 m0, s20
	s_nop 0
	global_load_lds_dwordx4 v[192:193], off
	s_waitcnt vmcnt(8)
	s_waitcnt lgkmcnt(0)
	s_barrier
	s_setprio 1
	s_waitcnt lgkmcnt(0)
	v_mfma_scale_f32_16x16x128_f8f6f4 v[94:97], v[26:33], v[200:207], v[94:97], v194, v169 op_sel_hi:[0,0,0]
	v_mfma_scale_f32_16x16x128_f8f6f4 v[86:89], v[18:25], v[200:207], v[86:89], v194, v169 op_sel_hi:[0,0,0]
	v_mfma_scale_f32_16x16x128_f8f6f4 v[78:81], v[26:33], v[208:215], v[78:81], v194, v169 op_sel_hi:[0,0,0]
	v_mfma_scale_f32_16x16x128_f8f6f4 v[70:73], v[18:25], v[208:215], v[70:73], v194, v169 op_sel_hi:[0,0,0]
	v_mfma_scale_f32_16x16x128_f8f6f4 v[62:65], v[26:33], v[216:223], v[62:65], v194, v169 op_sel_hi:[0,0,0]
	v_mfma_scale_f32_16x16x128_f8f6f4 v[54:57], v[18:25], v[216:223], v[54:57], v194, v169 op_sel_hi:[0,0,0]
	v_mfma_scale_f32_16x16x128_f8f6f4 v[46:49], v[26:33], v[236:243], v[46:49], v194, v169 op_sel_hi:[0,0,0]
	v_mfma_scale_f32_16x16x128_f8f6f4 v[38:41], v[18:25], v[236:243], v[38:41], v194, v169 op_sel_hi:[0,0,0]
	s_setprio 0
	s_setprio 1
	v_mfma_scale_f32_16x16x128_f8f6f4 v[90:93], v[10:17], v[200:207], v[90:93], v194, v169 op_sel_hi:[0,0,0]
	v_mfma_scale_f32_16x16x128_f8f6f4 v[82:85], v[2:9], v[200:207], v[82:85], v194, v169 op_sel_hi:[0,0,0]
	v_mfma_scale_f32_16x16x128_f8f6f4 v[74:77], v[10:17], v[208:215], v[74:77], v194, v169 op_sel_hi:[0,0,0]
	v_mfma_scale_f32_16x16x128_f8f6f4 v[66:69], v[2:9], v[208:215], v[66:69], v194, v169 op_sel_hi:[0,0,0]
	v_mfma_scale_f32_16x16x128_f8f6f4 v[58:61], v[10:17], v[216:223], v[58:61], v194, v169 op_sel_hi:[0,0,0]
	v_mfma_scale_f32_16x16x128_f8f6f4 v[50:53], v[2:9], v[216:223], v[50:53], v194, v169 op_sel_hi:[0,0,0]
	v_mfma_scale_f32_16x16x128_f8f6f4 v[42:45], v[10:17], v[236:243], v[42:45], v194, v169 op_sel_hi:[0,0,0]
	v_mfma_scale_f32_16x16x128_f8f6f4 v[34:37], v[2:9], v[236:243], v[34:37], v194, v169 op_sel_hi:[0,0,0]
	s_setprio 0
	s_barrier
	s_add_i32 s68, 0, 0x18000
	s_add_i32 s69, 0, 0x1c000
	v_add_u32_e32 v2, s68, v196
	v_add_u32_e32 v6, s69, v196
	ds_read_b128 v[26:29], v2
	ds_read_b128 v[30:33], v2 offset:1024
	ds_read_b128 v[18:21], v2 offset:2048
	ds_read_b128 v[22:25], v2 offset:3072
	ds_read_b128 v[10:13], v6
	ds_read_b128 v[14:17], v6 offset:1024
	ds_read_b128 v[2:5], v6 offset:2048
	ds_read_b128 v[6:9], v6 offset:3072
	s_add_u32 s58, s58, 0x20000
	s_addc_u32 s59, s59, 0
	s_mov_b32 m0, s21
	v_lshl_add_u64 v[170:171], s[58:59], 0, v[164:165]
	ds_read_b128 v[200:203], v198 offset:32768
	ds_read_b128 v[204:207], v198 offset:33792
	ds_read_b128 v[208:211], v198 offset:34816
	ds_read_b128 v[212:215], v198 offset:35840
	ds_read_b128 v[216:219], v198 offset:36864
	ds_read_b128 v[220:223], v198 offset:37888
	ds_read_b128 v[236:239], v198 offset:38912
	ds_read_b128 v[240:243], v198 offset:39936
	global_load_lds_dwordx4 v[170:171], off
	v_lshl_add_u64 v[170:171], s[58:59], 0, v[162:163]
	s_mov_b32 m0, s22
	s_nop 0
	global_load_lds_dwordx4 v[170:171], off
	s_waitcnt vmcnt(8)
	s_waitcnt lgkmcnt(0)
	s_barrier
	s_setprio 1
	s_waitcnt lgkmcnt(0)
	v_mfma_scale_f32_16x16x128_f8f6f4 v[158:161], v[26:33], v[200:207], v[158:161], v194, v169 op_sel_hi:[0,0,0]
	v_mfma_scale_f32_16x16x128_f8f6f4 v[150:153], v[18:25], v[200:207], v[150:153], v194, v169 op_sel_hi:[0,0,0]
	v_mfma_scale_f32_16x16x128_f8f6f4 v[142:145], v[26:33], v[208:215], v[142:145], v194, v169 op_sel_hi:[0,0,0]
	v_mfma_scale_f32_16x16x128_f8f6f4 v[134:137], v[18:25], v[208:215], v[134:137], v194, v169 op_sel_hi:[0,0,0]
	v_mfma_scale_f32_16x16x128_f8f6f4 v[126:129], v[26:33], v[216:223], v[126:129], v194, v169 op_sel_hi:[0,0,0]
	v_mfma_scale_f32_16x16x128_f8f6f4 v[118:121], v[18:25], v[216:223], v[118:121], v194, v169 op_sel_hi:[0,0,0]
	v_mfma_scale_f32_16x16x128_f8f6f4 v[110:113], v[26:33], v[236:243], v[110:113], v194, v169 op_sel_hi:[0,0,0]
	v_mfma_scale_f32_16x16x128_f8f6f4 v[102:105], v[18:25], v[236:243], v[102:105], v194, v169 op_sel_hi:[0,0,0]
	s_setprio 0
	s_setprio 1
	v_mfma_scale_f32_16x16x128_f8f6f4 v[154:157], v[10:17], v[200:207], v[154:157], v194, v169 op_sel_hi:[0,0,0]
	v_mfma_scale_f32_16x16x128_f8f6f4 v[146:149], v[2:9], v[200:207], v[146:149], v194, v169 op_sel_hi:[0,0,0]
	v_mfma_scale_f32_16x16x128_f8f6f4 v[138:141], v[10:17], v[208:215], v[138:141], v194, v169 op_sel_hi:[0,0,0]
	v_mfma_scale_f32_16x16x128_f8f6f4 v[130:133], v[2:9], v[208:215], v[130:133], v194, v169 op_sel_hi:[0,0,0]
	v_mfma_scale_f32_16x16x128_f8f6f4 v[122:125], v[10:17], v[216:223], v[122:125], v194, v169 op_sel_hi:[0,0,0]
	v_mfma_scale_f32_16x16x128_f8f6f4 v[114:117], v[2:9], v[216:223], v[114:117], v194, v169 op_sel_hi:[0,0,0]
	v_mfma_scale_f32_16x16x128_f8f6f4 v[106:109], v[10:17], v[236:243], v[106:109], v194, v169 op_sel_hi:[0,0,0]
	v_mfma_scale_f32_16x16x128_f8f6f4 v[98:101], v[2:9], v[236:243], v[98:101], v194, v169 op_sel_hi:[0,0,0]
	s_setprio 0
	s_barrier
	s_add_i32 s58, s68, s14
	v_lshl_add_u64 v[170:171], v[186:187], 0, s[56:57]
	s_mov_b32 m0, s58
	ds_read_b128 v[200:203], v198 offset:49152
	ds_read_b128 v[204:207], v198 offset:50176
	ds_read_b128 v[208:211], v198 offset:51200
	ds_read_b128 v[212:215], v198 offset:52224
	ds_read_b128 v[216:219], v198 offset:53248
	ds_read_b128 v[220:223], v198 offset:54272
	ds_read_b128 v[236:239], v198 offset:55296
	ds_read_b128 v[240:243], v198 offset:56320
	global_load_lds_dwordx4 v[170:171], off
	s_add_i32 m0, s58, 0x2000
	s_add_u32 s54, s54, 0x20080
	v_lshl_add_u64 v[170:171], v[188:189], 0, s[56:57]
	s_addc_u32 s55, s55, 0
	s_add_i32 s58, s69, s14
	global_load_lds_dwordx4 v[170:171], off
	v_lshl_add_u64 v[170:171], s[54:55], 0, v[166:167]
	s_mov_b32 m0, s58
	s_nop 0
	global_load_lds_dwordx4 v[170:171], off
	v_lshl_add_u64 v[170:171], s[54:55], 0, v[178:179]
	s_add_i32 m0, s58, 0x2000
	s_nop 0
	global_load_lds_dwordx4 v[170:171], off
	v_lshl_add_u64 v[170:171], v[190:191], 0, s[56:57]
	s_mov_b32 m0, s23
	s_nop 0
	global_load_lds_dwordx4 v[170:171], off
	v_lshl_add_u64 v[170:171], v[192:193], 0, s[56:57]
	s_mov_b32 m0, s24
	s_nop 0
	global_load_lds_dwordx4 v[170:171], off
	s_waitcnt vmcnt(8)
	s_waitcnt lgkmcnt(0)
	s_barrier
	s_setprio 1
	s_waitcnt lgkmcnt(0)
	v_mfma_scale_f32_16x16x128_f8f6f4 v[94:97], v[26:33], v[200:207], v[94:97], v194, v169 op_sel_hi:[0,0,0]
	v_mfma_scale_f32_16x16x128_f8f6f4 v[86:89], v[18:25], v[200:207], v[86:89], v194, v169 op_sel_hi:[0,0,0]
	v_mfma_scale_f32_16x16x128_f8f6f4 v[78:81], v[26:33], v[208:215], v[78:81], v194, v169 op_sel_hi:[0,0,0]
	v_mfma_scale_f32_16x16x128_f8f6f4 v[70:73], v[18:25], v[208:215], v[70:73], v194, v169 op_sel_hi:[0,0,0]
	v_mfma_scale_f32_16x16x128_f8f6f4 v[62:65], v[26:33], v[216:223], v[62:65], v194, v169 op_sel_hi:[0,0,0]
	v_mfma_scale_f32_16x16x128_f8f6f4 v[54:57], v[18:25], v[216:223], v[54:57], v194, v169 op_sel_hi:[0,0,0]
	v_mfma_scale_f32_16x16x128_f8f6f4 v[46:49], v[26:33], v[236:243], v[46:49], v194, v169 op_sel_hi:[0,0,0]
	v_mfma_scale_f32_16x16x128_f8f6f4 v[38:41], v[18:25], v[236:243], v[38:41], v194, v169 op_sel_hi:[0,0,0]
	s_setprio 0
	s_setprio 1
	v_mfma_scale_f32_16x16x128_f8f6f4 v[90:93], v[10:17], v[200:207], v[90:93], v194, v169 op_sel_hi:[0,0,0]
	v_mfma_scale_f32_16x16x128_f8f6f4 v[82:85], v[2:9], v[200:207], v[82:85], v194, v169 op_sel_hi:[0,0,0]
	v_mfma_scale_f32_16x16x128_f8f6f4 v[74:77], v[10:17], v[208:215], v[74:77], v194, v169 op_sel_hi:[0,0,0]
	v_mfma_scale_f32_16x16x128_f8f6f4 v[66:69], v[2:9], v[208:215], v[66:69], v194, v169 op_sel_hi:[0,0,0]
	v_mfma_scale_f32_16x16x128_f8f6f4 v[58:61], v[10:17], v[216:223], v[58:61], v194, v169 op_sel_hi:[0,0,0]
	v_mfma_scale_f32_16x16x128_f8f6f4 v[50:53], v[2:9], v[216:223], v[50:53], v194, v169 op_sel_hi:[0,0,0]
	v_mfma_scale_f32_16x16x128_f8f6f4 v[42:45], v[10:17], v[236:243], v[42:45], v194, v169 op_sel_hi:[0,0,0]
	v_mfma_scale_f32_16x16x128_f8f6f4 v[34:37], v[2:9], v[236:243], v[34:37], v194, v169 op_sel_hi:[0,0,0]
	s_setprio 0
	s_add_u32 s64, s64, 0x100
	s_addc_u32 s65, s65, 0
	s_add_u32 s52, s52, 0x100
	s_addc_u32 s53, s53, 0
	s_cmp_ge_i32 s66, s13
	s_mov_b32 s54, s66
	s_cbranch_scc1 .Lq4skip_ph7f
	s_barrier
	s_branch .LBB0_842
.Lq4skip_ph7f:
	s_nop 1
	s_mov_b64 s[70:71], 0xe800800
	v_mov_b32_e32 v209, v1
	s_and_b64 vcc, exec, s[36:37]
	s_cbranch_vccz .LBB0_845

.LBB0_1016:
	s_add_i32 s27, s37, 2
	s_add_u32 s40, s38, 0xfffe0080
	s_addc_u32 s41, s39, -1
	s_add_i32 s65, 0, 0x10000
	s_cmp_eq_u32 s95, s37
	s_cselect_b32 s69, s0, s41
	s_cselect_b32 s68, s1, s40
	s_cselect_b32 s41, s8, s19
	s_cselect_b32 s40, s11, s16
	s_add_i32 s37, 0, 0x14000
	v_add_u32_e32 v2, s65, v221
	v_add_u32_e32 v6, s37, v221
	ds_read_b128 v[26:29], v2
	ds_read_b128 v[30:33], v2 offset:1024
	ds_read_b128 v[18:21], v2 offset:2048
	ds_read_b128 v[22:25], v2 offset:3072
	ds_read_b128 v[10:13], v6
	ds_read_b128 v[14:17], v6 offset:1024
	ds_read_b128 v[2:5], v6 offset:2048
	ds_read_b128 v[6:9], v6 offset:3072
	v_lshl_add_u64 v[170:171], s[38:39], 0, v[192:193]
	s_add_i32 m0, s21, 0xc000
	ds_read_b128 v[194:197], v222
	ds_read_b128 v[198:201], v222 offset:1024
	ds_read_b128 v[202:205], v222 offset:2048
	ds_read_b128 v[206:209], v222 offset:3072
	ds_read_b128 v[210:213], v222 offset:4096
	ds_read_b128 v[214:217], v222 offset:5120
	ds_read_b128 v[236:239], v222 offset:6144
	ds_read_b128 v[240:243], v222 offset:7168
	global_load_lds_dwordx4 v[170:171], off
	v_lshl_add_u64 v[170:171], s[38:39], 0, v[190:191]
	s_add_i32 m0, s21, 0xe000
	s_nop 0
	global_load_lds_dwordx4 v[170:171], off
	s_waitcnt vmcnt(8)
	s_waitcnt lgkmcnt(0)
	s_barrier
	s_setprio 1
	s_waitcnt lgkmcnt(0)
	v_mfma_scale_f32_16x16x128_f8f6f4 v[94:97], v[26:33], v[194:201], v[94:97], v183, v169 op_sel_hi:[0,0,0]
	v_mfma_scale_f32_16x16x128_f8f6f4 v[90:93], v[18:25], v[194:201], v[90:93], v183, v169 op_sel_hi:[0,0,0]
	v_mfma_scale_f32_16x16x128_f8f6f4 v[86:89], v[26:33], v[202:209], v[86:89], v183, v169 op_sel_hi:[0,0,0]
	v_mfma_scale_f32_16x16x128_f8f6f4 v[82:85], v[18:25], v[202:209], v[82:85], v183, v169 op_sel_hi:[0,0,0]
	v_mfma_scale_f32_16x16x128_f8f6f4 v[78:81], v[26:33], v[210:217], v[78:81], v183, v169 op_sel_hi:[0,0,0]
	v_mfma_scale_f32_16x16x128_f8f6f4 v[74:77], v[18:25], v[210:217], v[74:77], v183, v169 op_sel_hi:[0,0,0]
	v_mfma_scale_f32_16x16x128_f8f6f4 v[70:73], v[26:33], v[236:243], v[70:73], v183, v169 op_sel_hi:[0,0,0]
	v_mfma_scale_f32_16x16x128_f8f6f4 v[66:69], v[18:25], v[236:243], v[66:69], v183, v169 op_sel_hi:[0,0,0]
	s_setprio 0
	s_setprio 1
	v_mfma_scale_f32_16x16x128_f8f6f4 v[158:161], v[10:17], v[194:201], v[158:161], v183, v169 op_sel_hi:[0,0,0]
	v_mfma_scale_f32_16x16x128_f8f6f4 v[154:157], v[2:9], v[194:201], v[154:157], v183, v169 op_sel_hi:[0,0,0]
	v_mfma_scale_f32_16x16x128_f8f6f4 v[150:153], v[10:17], v[202:209], v[150:153], v183, v169 op_sel_hi:[0,0,0]
	v_mfma_scale_f32_16x16x128_f8f6f4 v[146:149], v[2:9], v[202:209], v[146:149], v183, v169 op_sel_hi:[0,0,0]
	v_mfma_scale_f32_16x16x128_f8f6f4 v[142:145], v[10:17], v[210:217], v[142:145], v183, v169 op_sel_hi:[0,0,0]
	v_mfma_scale_f32_16x16x128_f8f6f4 v[138:141], v[2:9], v[210:217], v[138:141], v183, v169 op_sel_hi:[0,0,0]
	v_mfma_scale_f32_16x16x128_f8f6f4 v[134:137], v[10:17], v[236:243], v[134:137], v183, v169 op_sel_hi:[0,0,0]
	v_mfma_scale_f32_16x16x128_f8f6f4 v[130:133], v[2:9], v[236:243], v[130:133], v183, v169 op_sel_hi:[0,0,0]
	s_setprio 0
	s_barrier
	s_add_i32 s65, s65, s20
	v_lshl_add_u64 v[194:195], s[40:41], 0, v[162:163]
	s_mov_b32 m0, s65
	ds_read_b128 v[202:205], v222 offset:16384
	ds_read_b128 v[206:209], v222 offset:17408
	ds_read_b128 v[210:213], v222 offset:18432
	ds_read_b128 v[214:217], v222 offset:19456
	ds_read_b128 v[236:239], v222 offset:20480
	ds_read_b128 v[240:243], v222 offset:21504
	ds_read_b128 v[244:247], v222 offset:22528
	ds_read_b128 v[248:251], v222 offset:23552
	global_load_lds_dwordx4 v[194:195], off
	s_add_i32 m0, s65, 0x2000
	s_add_u32 s70, s40, 0x20000
	v_lshl_add_u64 v[196:197], s[40:41], 0, v[164:165]
	s_addc_u32 s71, s41, 0
	s_add_i32 s37, s37, s20
	global_load_lds_dwordx4 v[196:197], off
	v_lshl_add_u64 v[170:171], s[70:71], 0, v[162:163]
	s_mov_b32 m0, s37
	v_lshl_add_u64 v[198:199], s[68:69], 0, v[178:179]
	global_load_lds_dwordx4 v[170:171], off
	v_lshl_add_u64 v[170:171], s[70:71], 0, v[164:165]
	s_add_i32 m0, s37, 0x2000
	v_lshl_add_u64 v[200:201], s[68:69], 0, v[180:181]
	global_load_lds_dwordx4 v[170:171], off
	s_mov_b32 m0, s21
	s_nop 0
	global_load_lds_dwordx4 v[198:199], off
	s_mov_b32 m0, s22
	s_nop 0
	global_load_lds_dwordx4 v[200:201], off
	s_waitcnt vmcnt(8)
	s_waitcnt lgkmcnt(0)
	s_barrier
	s_setprio 1
	s_waitcnt lgkmcnt(0)
	v_mfma_scale_f32_16x16x128_f8f6f4 v[62:65], v[26:33], v[202:209], v[62:65], v183, v169 op_sel_hi:[0,0,0]
	v_mfma_scale_f32_16x16x128_f8f6f4 v[58:61], v[18:25], v[202:209], v[58:61], v183, v169 op_sel_hi:[0,0,0]
	v_mfma_scale_f32_16x16x128_f8f6f4 v[54:57], v[26:33], v[210:217], v[54:57], v183, v169 op_sel_hi:[0,0,0]
	v_mfma_scale_f32_16x16x128_f8f6f4 v[50:53], v[18:25], v[210:217], v[50:53], v183, v169 op_sel_hi:[0,0,0]
	v_mfma_scale_f32_16x16x128_f8f6f4 v[46:49], v[26:33], v[236:243], v[46:49], v183, v169 op_sel_hi:[0,0,0]
	v_mfma_scale_f32_16x16x128_f8f6f4 v[42:45], v[18:25], v[236:243], v[42:45], v183, v169 op_sel_hi:[0,0,0]
	v_mfma_scale_f32_16x16x128_f8f6f4 v[38:41], v[26:33], v[244:251], v[38:41], v183, v169 op_sel_hi:[0,0,0]
	v_mfma_scale_f32_16x16x128_f8f6f4 v[34:37], v[18:25], v[244:251], v[34:37], v183, v169 op_sel_hi:[0,0,0]
	s_setprio 0
	s_setprio 1
	v_mfma_scale_f32_16x16x128_f8f6f4 v[126:129], v[10:17], v[202:209], v[126:129], v183, v169 op_sel_hi:[0,0,0]
	v_mfma_scale_f32_16x16x128_f8f6f4 v[122:125], v[2:9], v[202:209], v[122:125], v183, v169 op_sel_hi:[0,0,0]
	v_mfma_scale_f32_16x16x128_f8f6f4 v[118:121], v[10:17], v[210:217], v[118:121], v183, v169 op_sel_hi:[0,0,0]
	v_mfma_scale_f32_16x16x128_f8f6f4 v[114:117], v[2:9], v[210:217], v[114:117], v183, v169 op_sel_hi:[0,0,0]
	v_mfma_scale_f32_16x16x128_f8f6f4 v[110:113], v[10:17], v[236:243], v[110:113], v183, v169 op_sel_hi:[0,0,0]
	v_mfma_scale_f32_16x16x128_f8f6f4 v[106:109], v[2:9], v[236:243], v[106:109], v183, v169 op_sel_hi:[0,0,0]
	v_mfma_scale_f32_16x16x128_f8f6f4 v[102:105], v[10:17], v[244:251], v[102:105], v183, v169 op_sel_hi:[0,0,0]
	v_mfma_scale_f32_16x16x128_f8f6f4 v[98:101], v[2:9], v[244:251], v[98:101], v183, v169 op_sel_hi:[0,0,0]
	s_setprio 0
	s_barrier
	s_add_i32 s37, 0, 0x18000
	s_add_i32 s65, 0, 0x1c000
	v_add_u32_e32 v2, s37, v221
	v_add_u32_e32 v6, s65, v221
	ds_read_b128 v[26:29], v2
	ds_read_b128 v[30:33], v2 offset:1024
	ds_read_b128 v[18:21], v2 offset:2048
	ds_read_b128 v[22:25], v2 offset:3072
	ds_read_b128 v[10:13], v6
	ds_read_b128 v[14:17], v6 offset:1024
	ds_read_b128 v[2:5], v6 offset:2048
	ds_read_b128 v[6:9], v6 offset:3072
	s_add_u32 s68, s68, 0x20000
	s_addc_u32 s69, s69, 0
	s_mov_b32 m0, s23
	v_lshl_add_u64 v[170:171], s[68:69], 0, v[178:179]
	ds_read_b128 v[202:205], v222 offset:32768
	ds_read_b128 v[206:209], v222 offset:33792
	ds_read_b128 v[210:213], v222 offset:34816
	ds_read_b128 v[214:217], v222 offset:35840
	ds_read_b128 v[236:239], v222 offset:36864
	ds_read_b128 v[240:243], v222 offset:37888
	ds_read_b128 v[244:247], v222 offset:38912
	ds_read_b128 v[248:251], v222 offset:39936
	global_load_lds_dwordx4 v[170:171], off
	v_lshl_add_u64 v[170:171], s[68:69], 0, v[180:181]
	s_mov_b32 m0, s12
	s_nop 0
	global_load_lds_dwordx4 v[170:171], off
	s_waitcnt vmcnt(8)
	s_waitcnt lgkmcnt(0)
	s_barrier
	s_setprio 1
	s_waitcnt lgkmcnt(0)
	v_mfma_scale_f32_16x16x128_f8f6f4 v[94:97], v[26:33], v[202:209], v[94:97], v183, v169 op_sel_hi:[0,0,0]
	v_mfma_scale_f32_16x16x128_f8f6f4 v[90:93], v[18:25], v[202:209], v[90:93], v183, v169 op_sel_hi:[0,0,0]
	v_mfma_scale_f32_16x16x128_f8f6f4 v[86:89], v[26:33], v[210:217], v[86:89], v183, v169 op_sel_hi:[0,0,0]
	v_mfma_scale_f32_16x16x128_f8f6f4 v[82:85], v[18:25], v[210:217], v[82:85], v183, v169 op_sel_hi:[0,0,0]
	v_mfma_scale_f32_16x16x128_f8f6f4 v[78:81], v[26:33], v[236:243], v[78:81], v183, v169 op_sel_hi:[0,0,0]
	v_mfma_scale_f32_16x16x128_f8f6f4 v[74:77], v[18:25], v[236:243], v[74:77], v183, v169 op_sel_hi:[0,0,0]
	v_mfma_scale_f32_16x16x128_f8f6f4 v[70:73], v[26:33], v[244:251], v[70:73], v183, v169 op_sel_hi:[0,0,0]
	v_mfma_scale_f32_16x16x128_f8f6f4 v[66:69], v[18:25], v[244:251], v[66:69], v183, v169 op_sel_hi:[0,0,0]
	s_setprio 0
	s_setprio 1
	v_mfma_scale_f32_16x16x128_f8f6f4 v[158:161], v[10:17], v[202:209], v[158:161], v183, v169 op_sel_hi:[0,0,0]
	v_mfma_scale_f32_16x16x128_f8f6f4 v[154:157], v[2:9], v[202:209], v[154:157], v183, v169 op_sel_hi:[0,0,0]
	v_mfma_scale_f32_16x16x128_f8f6f4 v[150:153], v[10:17], v[210:217], v[150:153], v183, v169 op_sel_hi:[0,0,0]
	v_mfma_scale_f32_16x16x128_f8f6f4 v[146:149], v[2:9], v[210:217], v[146:149], v183, v169 op_sel_hi:[0,0,0]
	v_mfma_scale_f32_16x16x128_f8f6f4 v[142:145], v[10:17], v[236:243], v[142:145], v183, v169 op_sel_hi:[0,0,0]
	v_mfma_scale_f32_16x16x128_f8f6f4 v[138:141], v[2:9], v[236:243], v[138:141], v183, v169 op_sel_hi:[0,0,0]
	v_mfma_scale_f32_16x16x128_f8f6f4 v[134:137], v[10:17], v[244:251], v[134:137], v183, v169 op_sel_hi:[0,0,0]
	v_mfma_scale_f32_16x16x128_f8f6f4 v[130:133], v[2:9], v[244:251], v[130:133], v183, v169 op_sel_hi:[0,0,0]
	s_setprio 0
	s_barrier
	s_add_i32 s37, s37, s20
	v_lshl_add_u64 v[170:171], v[194:195], 0, s[56:57]
	s_mov_b32 m0, s37
	ds_read_b128 v[202:205], v222 offset:49152
	ds_read_b128 v[206:209], v222 offset:50176
	ds_read_b128 v[210:213], v222 offset:51200
	ds_read_b128 v[214:217], v222 offset:52224
	ds_read_b128 v[236:239], v222 offset:53248
	ds_read_b128 v[240:243], v222 offset:54272
	ds_read_b128 v[244:247], v222 offset:55296
	ds_read_b128 v[248:251], v222 offset:56320
	global_load_lds_dwordx4 v[170:171], off
	s_add_i32 m0, s37, 0x2000
	s_add_u32 s40, s40, 0x20080
	v_lshl_add_u64 v[170:171], v[196:197], 0, s[56:57]
	s_addc_u32 s41, s41, 0
	s_add_i32 s37, s65, s20
	global_load_lds_dwordx4 v[170:171], off
	v_lshl_add_u64 v[170:171], s[40:41], 0, v[162:163]
	s_mov_b32 m0, s37
	s_nop 0
	global_load_lds_dwordx4 v[170:171], off
	v_lshl_add_u64 v[170:171], s[40:41], 0, v[164:165]
	s_add_i32 m0, s37, 0x2000
	s_nop 0
	global_load_lds_dwordx4 v[170:171], off
	v_lshl_add_u64 v[170:171], v[198:199], 0, s[56:57]
	s_mov_b32 m0, s92
	s_nop 0
	global_load_lds_dwordx4 v[170:171], off
	v_lshl_add_u64 v[170:171], v[200:201], 0, s[56:57]
	s_mov_b32 m0, s93
	s_nop 0
	global_load_lds_dwordx4 v[170:171], off
	s_waitcnt vmcnt(8)
	s_waitcnt lgkmcnt(0)
	s_barrier
	s_setprio 1
	s_waitcnt lgkmcnt(0)
	v_mfma_scale_f32_16x16x128_f8f6f4 v[62:65], v[26:33], v[202:209], v[62:65], v183, v169 op_sel_hi:[0,0,0]
	v_mfma_scale_f32_16x16x128_f8f6f4 v[58:61], v[18:25], v[202:209], v[58:61], v183, v169 op_sel_hi:[0,0,0]
	v_mfma_scale_f32_16x16x128_f8f6f4 v[54:57], v[26:33], v[210:217], v[54:57], v183, v169 op_sel_hi:[0,0,0]
	v_mfma_scale_f32_16x16x128_f8f6f4 v[50:53], v[18:25], v[210:217], v[50:53], v183, v169 op_sel_hi:[0,0,0]
	v_mfma_scale_f32_16x16x128_f8f6f4 v[46:49], v[26:33], v[236:243], v[46:49], v183, v169 op_sel_hi:[0,0,0]
	v_mfma_scale_f32_16x16x128_f8f6f4 v[42:45], v[18:25], v[236:243], v[42:45], v183, v169 op_sel_hi:[0,0,0]
	v_mfma_scale_f32_16x16x128_f8f6f4 v[38:41], v[26:33], v[244:251], v[38:41], v183, v169 op_sel_hi:[0,0,0]
	v_mfma_scale_f32_16x16x128_f8f6f4 v[34:37], v[18:25], v[244:251], v[34:37], v183, v169 op_sel_hi:[0,0,0]
	s_setprio 0
	s_setprio 1
	v_mfma_scale_f32_16x16x128_f8f6f4 v[126:129], v[10:17], v[202:209], v[126:129], v183, v169 op_sel_hi:[0,0,0]
	v_mfma_scale_f32_16x16x128_f8f6f4 v[122:125], v[2:9], v[202:209], v[122:125], v183, v169 op_sel_hi:[0,0,0]
	v_mfma_scale_f32_16x16x128_f8f6f4 v[118:121], v[10:17], v[210:217], v[118:121], v183, v169 op_sel_hi:[0,0,0]
	v_mfma_scale_f32_16x16x128_f8f6f4 v[114:117], v[2:9], v[210:217], v[114:117], v183, v169 op_sel_hi:[0,0,0]
	v_mfma_scale_f32_16x16x128_f8f6f4 v[110:113], v[10:17], v[236:243], v[110:113], v183, v169 op_sel_hi:[0,0,0]
	v_mfma_scale_f32_16x16x128_f8f6f4 v[106:109], v[2:9], v[236:243], v[106:109], v183, v169 op_sel_hi:[0,0,0]
	v_mfma_scale_f32_16x16x128_f8f6f4 v[102:105], v[10:17], v[244:251], v[102:105], v183, v169 op_sel_hi:[0,0,0]
	v_mfma_scale_f32_16x16x128_f8f6f4 v[98:101], v[2:9], v[244:251], v[98:101], v183, v169 op_sel_hi:[0,0,0]
	s_setprio 0
	s_add_u32 s16, s16, 0x100
	s_addc_u32 s19, s19, 0
	s_add_u32 s38, s38, 0x100
	s_addc_u32 s39, s39, 0
	s_cmp_ge_i32 s27, s74
	s_mov_b32 s37, s27
	s_cbranch_scc1 .Lq4skip_ph9
	s_barrier
	s_branch .LBB0_1016
.Lq4skip_ph9:
	s_nop 1
	s_mov_b64 s[70:71], 0xe800800
	v_mov_b32_e32 v209, v1
	s_and_b64 vcc, exec, s[52:53]
	s_cbranch_vccz .LBB0_1019

.LBB0_1438:
	s_add_i32 s66, s54, 2
	s_add_u32 s55, s52, 0xfffc0080
	s_addc_u32 s58, s53, -1
	s_add_i32 s68, 0, 0x10000
	s_cmp_eq_u32 s60, s54
	s_cselect_b32 s59, s41, s58
	s_cselect_b32 s58, s43, s55
	v_add_u32_e32 v144, s68, v147
	s_cselect_b32 s55, s62, s65
	s_cselect_b32 s54, s63, s64
	s_add_i32 s70, 0, 0x14000
	ds_read_b128 v[140:143], v144
	ds_read_b128 v[150:153], v144 offset:1024
	ds_read_b128 v[154:157], v144 offset:2048
	ds_read_b128 v[158:161], v144 offset:3072
	v_add_u32_e32 v144, s70, v147
	ds_read_b128 v[162:165], v144
	ds_read_b128 v[170:173], v144 offset:1024
	ds_read_b128 v[174:177], v144 offset:2048
	ds_read_b128 v[178:181], v144 offset:3072
	v_lshl_add_u64 v[144:145], s[52:53], 0, v[138:139]
	s_add_i32 m0, s16, 0xc000
	ds_read_b128 v[182:185], v149
	ds_read_b128 v[186:189], v149 offset:1024
	ds_read_b128 v[190:193], v149 offset:2048
	ds_read_b128 v[194:197], v149 offset:3072
	ds_read_b128 v[198:201], v149 offset:4096
	ds_read_b128 v[202:205], v149 offset:5120
	ds_read_b128 v[206:209], v149 offset:6144
	ds_read_b128 v[210:213], v149 offset:7168
	global_load_lds_dwordx4 v[144:145], off
	v_lshl_add_u64 v[144:145], s[52:53], 0, v[136:137]
	s_add_i32 m0, s16, 0xe000
	s_nop 0
	global_load_lds_dwordx4 v[144:145], off
	s_waitcnt vmcnt(8)
	s_waitcnt lgkmcnt(0)
	s_barrier
	s_setprio 1
	s_waitcnt lgkmcnt(0)
	v_mfma_f32_16x16x32_bf16 v[126:129], v[140:143], v[182:185], v[126:129]
	v_mfma_f32_16x16x32_bf16 v[122:125], v[154:157], v[182:185], v[122:125]
	v_mfma_f32_16x16x32_bf16 v[110:113], v[140:143], v[190:193], v[110:113]
	v_mfma_f32_16x16x32_bf16 v[106:109], v[154:157], v[190:193], v[106:109]
	v_mfma_f32_16x16x32_bf16 v[94:97], v[140:143], v[198:201], v[94:97]
	v_mfma_f32_16x16x32_bf16 v[90:93], v[154:157], v[198:201], v[90:93]
	v_mfma_f32_16x16x32_bf16 v[78:81], v[140:143], v[206:209], v[78:81]
	v_mfma_f32_16x16x32_bf16 v[74:77], v[154:157], v[206:209], v[74:77]
	v_mfma_f32_16x16x32_bf16 v[126:129], v[150:153], v[186:189], v[126:129]
	v_mfma_f32_16x16x32_bf16 v[122:125], v[158:161], v[186:189], v[122:125]
	v_mfma_f32_16x16x32_bf16 v[110:113], v[150:153], v[194:197], v[110:113]
	v_mfma_f32_16x16x32_bf16 v[106:109], v[158:161], v[194:197], v[106:109]
	v_mfma_f32_16x16x32_bf16 v[94:97], v[150:153], v[202:205], v[94:97]
	v_mfma_f32_16x16x32_bf16 v[90:93], v[158:161], v[202:205], v[90:93]
	v_mfma_f32_16x16x32_bf16 v[78:81], v[150:153], v[210:213], v[78:81]
	v_mfma_f32_16x16x32_bf16 v[74:77], v[158:161], v[210:213], v[74:77]
	s_setprio 0
	s_setprio 1
	v_mfma_f32_16x16x32_bf16 v[118:121], v[162:165], v[182:185], v[118:121]
	v_mfma_f32_16x16x32_bf16 v[114:117], v[174:177], v[182:185], v[114:117]
	v_mfma_f32_16x16x32_bf16 v[102:105], v[162:165], v[190:193], v[102:105]
	v_mfma_f32_16x16x32_bf16 v[98:101], v[174:177], v[190:193], v[98:101]
	v_mfma_f32_16x16x32_bf16 v[86:89], v[162:165], v[198:201], v[86:89]
	v_mfma_f32_16x16x32_bf16 v[82:85], v[174:177], v[198:201], v[82:85]
	v_mfma_f32_16x16x32_bf16 v[70:73], v[162:165], v[206:209], v[70:73]
	v_mfma_f32_16x16x32_bf16 v[66:69], v[174:177], v[206:209], v[66:69]
	v_mfma_f32_16x16x32_bf16 v[118:121], v[170:173], v[186:189], v[118:121]
	v_mfma_f32_16x16x32_bf16 v[114:117], v[178:181], v[186:189], v[114:117]
	v_mfma_f32_16x16x32_bf16 v[102:105], v[170:173], v[194:197], v[102:105]
	v_mfma_f32_16x16x32_bf16 v[98:101], v[178:181], v[194:197], v[98:101]
	v_mfma_f32_16x16x32_bf16 v[86:89], v[170:173], v[202:205], v[86:89]
	v_mfma_f32_16x16x32_bf16 v[82:85], v[178:181], v[202:205], v[82:85]
	v_mfma_f32_16x16x32_bf16 v[70:73], v[170:173], v[210:213], v[70:73]
	v_mfma_f32_16x16x32_bf16 v[66:69], v[178:181], v[210:213], v[66:69]
	s_setprio 0
	s_barrier
	s_add_i32 s68, s68, s15
	v_lshl_add_u64 v[144:145], s[54:55], 0, v[166:167]
	s_mov_b32 m0, s68
	ds_read_b128 v[182:185], v149 offset:16384
	ds_read_b128 v[186:189], v149 offset:17408
	ds_read_b128 v[190:193], v149 offset:18432
	ds_read_b128 v[194:197], v149 offset:19456
	ds_read_b128 v[198:201], v149 offset:20480
	ds_read_b128 v[202:205], v149 offset:21504
	ds_read_b128 v[206:209], v149 offset:22528
	ds_read_b128 v[210:213], v149 offset:23552
	global_load_lds_dwordx4 v[144:145], off
	s_add_i32 m0, s68, 0x2000
	s_add_u32 s68, s54, 0x40000
	v_lshl_add_u64 v[214:215], s[54:55], 0, v[130:131]
	s_addc_u32 s69, s55, 0
	s_add_i32 s70, s70, s15
	global_load_lds_dwordx4 v[214:215], off
	v_lshl_add_u64 v[216:217], s[68:69], 0, v[166:167]
	s_mov_b32 m0, s70
	v_lshl_add_u64 v[218:219], s[58:59], 0, v[134:135]
	global_load_lds_dwordx4 v[216:217], off
	v_lshl_add_u64 v[216:217], s[68:69], 0, v[130:131]
	s_add_i32 m0, s70, 0x2000
	s_nop 0
	global_load_lds_dwordx4 v[216:217], off
	v_lshl_add_u64 v[216:217], s[58:59], 0, v[132:133]
	s_mov_b32 m0, s16
	s_nop 0
	global_load_lds_dwordx4 v[216:217], off
	s_mov_b32 m0, s20
	s_nop 0
	global_load_lds_dwordx4 v[218:219], off
	s_waitcnt vmcnt(8)
	s_waitcnt lgkmcnt(0)
	s_barrier
	s_setprio 1
	s_waitcnt lgkmcnt(0)
	v_mfma_f32_16x16x32_bf16 v[62:65], v[140:143], v[182:185], v[62:65]
	v_mfma_f32_16x16x32_bf16 v[58:61], v[154:157], v[182:185], v[58:61]
	v_mfma_f32_16x16x32_bf16 v[46:49], v[140:143], v[190:193], v[46:49]
	v_mfma_f32_16x16x32_bf16 v[42:45], v[154:157], v[190:193], v[42:45]
	v_mfma_f32_16x16x32_bf16 v[30:33], v[140:143], v[198:201], v[30:33]
	v_mfma_f32_16x16x32_bf16 v[26:29], v[154:157], v[198:201], v[26:29]
	v_mfma_f32_16x16x32_bf16 v[14:17], v[140:143], v[206:209], v[14:17]
	v_mfma_f32_16x16x32_bf16 v[10:13], v[154:157], v[206:209], v[10:13]
	v_mfma_f32_16x16x32_bf16 v[62:65], v[150:153], v[186:189], v[62:65]
	v_mfma_f32_16x16x32_bf16 v[58:61], v[158:161], v[186:189], v[58:61]
	v_mfma_f32_16x16x32_bf16 v[46:49], v[150:153], v[194:197], v[46:49]
	v_mfma_f32_16x16x32_bf16 v[42:45], v[158:161], v[194:197], v[42:45]
	v_mfma_f32_16x16x32_bf16 v[30:33], v[150:153], v[202:205], v[30:33]
	v_mfma_f32_16x16x32_bf16 v[26:29], v[158:161], v[202:205], v[26:29]
	v_mfma_f32_16x16x32_bf16 v[14:17], v[150:153], v[210:213], v[14:17]
	v_mfma_f32_16x16x32_bf16 v[10:13], v[158:161], v[210:213], v[10:13]
	s_setprio 0
	s_setprio 1
	v_mfma_f32_16x16x32_bf16 v[54:57], v[162:165], v[182:185], v[54:57]
	v_mfma_f32_16x16x32_bf16 v[50:53], v[174:177], v[182:185], v[50:53]
	v_mfma_f32_16x16x32_bf16 v[38:41], v[162:165], v[190:193], v[38:41]
	v_mfma_f32_16x16x32_bf16 v[34:37], v[174:177], v[190:193], v[34:37]
	v_mfma_f32_16x16x32_bf16 v[22:25], v[162:165], v[198:201], v[22:25]
	v_mfma_f32_16x16x32_bf16 v[18:21], v[174:177], v[198:201], v[18:21]
	v_mfma_f32_16x16x32_bf16 v[6:9], v[162:165], v[206:209], v[6:9]
	v_mfma_f32_16x16x32_bf16 v[2:5], v[174:177], v[206:209], v[2:5]
	v_mfma_f32_16x16x32_bf16 v[54:57], v[170:173], v[186:189], v[54:57]
	v_mfma_f32_16x16x32_bf16 v[50:53], v[178:181], v[186:189], v[50:53]
	v_mfma_f32_16x16x32_bf16 v[38:41], v[170:173], v[194:197], v[38:41]
	v_mfma_f32_16x16x32_bf16 v[34:37], v[178:181], v[194:197], v[34:37]
	v_mfma_f32_16x16x32_bf16 v[22:25], v[170:173], v[202:205], v[22:25]
	v_mfma_f32_16x16x32_bf16 v[18:21], v[178:181], v[202:205], v[18:21]
	v_mfma_f32_16x16x32_bf16 v[6:9], v[170:173], v[210:213], v[6:9]
	v_mfma_f32_16x16x32_bf16 v[2:5], v[178:181], v[210:213], v[2:5]
	s_setprio 0
	s_barrier
	s_add_i32 s68, 0, 0x18000
	s_add_i32 s69, 0, 0x1c000
	v_add_u32_e32 v158, s68, v147
	v_add_u32_e32 v169, s69, v147
	ds_read_b128 v[140:143], v158
	ds_read_b128 v[150:153], v158 offset:1024
	ds_read_b128 v[154:157], v158 offset:2048
	ds_read_b128 v[158:161], v158 offset:3072
	ds_read_b128 v[162:165], v169
	ds_read_b128 v[170:173], v169 offset:1024
	ds_read_b128 v[174:177], v169 offset:2048
	ds_read_b128 v[178:181], v169 offset:3072
	s_add_u32 s58, s58, 0x40000
	s_addc_u32 s59, s59, 0
	s_mov_b32 m0, s21
	v_lshl_add_u64 v[220:221], s[58:59], 0, v[132:133]
	ds_read_b128 v[182:185], v149 offset:32768
	ds_read_b128 v[186:189], v149 offset:33792
	ds_read_b128 v[190:193], v149 offset:34816
	ds_read_b128 v[194:197], v149 offset:35840
	ds_read_b128 v[198:201], v149 offset:36864
	ds_read_b128 v[202:205], v149 offset:37888
	ds_read_b128 v[206:209], v149 offset:38912
	ds_read_b128 v[210:213], v149 offset:39936
	global_load_lds_dwordx4 v[220:221], off
	v_lshl_add_u64 v[220:221], s[58:59], 0, v[134:135]
	s_mov_b32 m0, s22
	s_nop 0
	global_load_lds_dwordx4 v[220:221], off
	s_waitcnt vmcnt(8)
	s_waitcnt lgkmcnt(0)
	s_barrier
	s_setprio 1
	s_waitcnt lgkmcnt(0)
	v_mfma_f32_16x16x32_bf16 v[126:129], v[140:143], v[182:185], v[126:129]
	v_mfma_f32_16x16x32_bf16 v[122:125], v[154:157], v[182:185], v[122:125]
	v_mfma_f32_16x16x32_bf16 v[110:113], v[140:143], v[190:193], v[110:113]
	v_mfma_f32_16x16x32_bf16 v[106:109], v[154:157], v[190:193], v[106:109]
	v_mfma_f32_16x16x32_bf16 v[94:97], v[140:143], v[198:201], v[94:97]
	v_mfma_f32_16x16x32_bf16 v[90:93], v[154:157], v[198:201], v[90:93]
	v_mfma_f32_16x16x32_bf16 v[78:81], v[140:143], v[206:209], v[78:81]
	v_mfma_f32_16x16x32_bf16 v[74:77], v[154:157], v[206:209], v[74:77]
	v_mfma_f32_16x16x32_bf16 v[126:129], v[150:153], v[186:189], v[126:129]
	v_mfma_f32_16x16x32_bf16 v[122:125], v[158:161], v[186:189], v[122:125]
	v_mfma_f32_16x16x32_bf16 v[110:113], v[150:153], v[194:197], v[110:113]
	v_mfma_f32_16x16x32_bf16 v[106:109], v[158:161], v[194:197], v[106:109]
	v_mfma_f32_16x16x32_bf16 v[94:97], v[150:153], v[202:205], v[94:97]
	v_mfma_f32_16x16x32_bf16 v[90:93], v[158:161], v[202:205], v[90:93]
	v_mfma_f32_16x16x32_bf16 v[78:81], v[150:153], v[210:213], v[78:81]
	v_mfma_f32_16x16x32_bf16 v[74:77], v[158:161], v[210:213], v[74:77]
	s_setprio 0
	s_setprio 1
	v_mfma_f32_16x16x32_bf16 v[118:121], v[162:165], v[182:185], v[118:121]
	v_mfma_f32_16x16x32_bf16 v[114:117], v[174:177], v[182:185], v[114:117]
	v_mfma_f32_16x16x32_bf16 v[102:105], v[162:165], v[190:193], v[102:105]
	v_mfma_f32_16x16x32_bf16 v[98:101], v[174:177], v[190:193], v[98:101]
	v_mfma_f32_16x16x32_bf16 v[86:89], v[162:165], v[198:201], v[86:89]
	v_mfma_f32_16x16x32_bf16 v[82:85], v[174:177], v[198:201], v[82:85]
	v_mfma_f32_16x16x32_bf16 v[70:73], v[162:165], v[206:209], v[70:73]
	v_mfma_f32_16x16x32_bf16 v[66:69], v[174:177], v[206:209], v[66:69]
	v_mfma_f32_16x16x32_bf16 v[118:121], v[170:173], v[186:189], v[118:121]
	v_mfma_f32_16x16x32_bf16 v[114:117], v[178:181], v[186:189], v[114:117]
	v_mfma_f32_16x16x32_bf16 v[102:105], v[170:173], v[194:197], v[102:105]
	v_mfma_f32_16x16x32_bf16 v[98:101], v[178:181], v[194:197], v[98:101]
	v_mfma_f32_16x16x32_bf16 v[86:89], v[170:173], v[202:205], v[86:89]
	v_mfma_f32_16x16x32_bf16 v[82:85], v[178:181], v[202:205], v[82:85]
	v_mfma_f32_16x16x32_bf16 v[70:73], v[170:173], v[210:213], v[70:73]
	v_mfma_f32_16x16x32_bf16 v[66:69], v[178:181], v[210:213], v[66:69]
	s_setprio 0
	s_barrier
	s_add_i32 s58, s68, s15
	v_lshl_add_u64 v[144:145], v[144:145], 0, s[56:57]
	s_mov_b32 m0, s58
	ds_read_b128 v[182:185], v149 offset:49152
	ds_read_b128 v[186:189], v149 offset:50176
	ds_read_b128 v[190:193], v149 offset:51200
	ds_read_b128 v[194:197], v149 offset:52224
	ds_read_b128 v[198:201], v149 offset:53248
	ds_read_b128 v[202:205], v149 offset:54272
	ds_read_b128 v[206:209], v149 offset:55296
	ds_read_b128 v[210:213], v149 offset:56320
	global_load_lds_dwordx4 v[144:145], off
	s_add_i32 m0, s58, 0x2000
	s_add_u32 s54, s54, 0x40080
	v_lshl_add_u64 v[144:145], v[214:215], 0, s[56:57]
	s_addc_u32 s55, s55, 0
	s_add_i32 s58, s69, s15
	global_load_lds_dwordx4 v[144:145], off
	v_lshl_add_u64 v[144:145], s[54:55], 0, v[166:167]
	s_mov_b32 m0, s58
	s_nop 0
	global_load_lds_dwordx4 v[144:145], off
	v_lshl_add_u64 v[144:145], s[54:55], 0, v[130:131]
	s_add_i32 m0, s58, 0x2000
	s_nop 0
	global_load_lds_dwordx4 v[144:145], off
	v_lshl_add_u64 v[144:145], v[216:217], 0, s[56:57]
	s_mov_b32 m0, s23
	s_nop 0
	global_load_lds_dwordx4 v[144:145], off
	v_lshl_add_u64 v[144:145], v[218:219], 0, s[56:57]
	s_mov_b32 m0, s24
	s_nop 0
	global_load_lds_dwordx4 v[144:145], off
	s_waitcnt vmcnt(8)
	s_waitcnt lgkmcnt(0)
	s_barrier
	s_setprio 1
	s_waitcnt lgkmcnt(0)
	v_mfma_f32_16x16x32_bf16 v[62:65], v[140:143], v[182:185], v[62:65]
	v_mfma_f32_16x16x32_bf16 v[58:61], v[154:157], v[182:185], v[58:61]
	v_mfma_f32_16x16x32_bf16 v[46:49], v[140:143], v[190:193], v[46:49]
	v_mfma_f32_16x16x32_bf16 v[42:45], v[154:157], v[190:193], v[42:45]
	v_mfma_f32_16x16x32_bf16 v[30:33], v[140:143], v[198:201], v[30:33]
	v_mfma_f32_16x16x32_bf16 v[26:29], v[154:157], v[198:201], v[26:29]
	v_mfma_f32_16x16x32_bf16 v[14:17], v[140:143], v[206:209], v[14:17]
	v_mfma_f32_16x16x32_bf16 v[10:13], v[154:157], v[206:209], v[10:13]
	v_mfma_f32_16x16x32_bf16 v[62:65], v[150:153], v[186:189], v[62:65]
	v_mfma_f32_16x16x32_bf16 v[58:61], v[158:161], v[186:189], v[58:61]
	v_mfma_f32_16x16x32_bf16 v[46:49], v[150:153], v[194:197], v[46:49]
	v_mfma_f32_16x16x32_bf16 v[42:45], v[158:161], v[194:197], v[42:45]
	v_mfma_f32_16x16x32_bf16 v[30:33], v[150:153], v[202:205], v[30:33]
	v_mfma_f32_16x16x32_bf16 v[26:29], v[158:161], v[202:205], v[26:29]
	v_mfma_f32_16x16x32_bf16 v[14:17], v[150:153], v[210:213], v[14:17]
	v_mfma_f32_16x16x32_bf16 v[10:13], v[158:161], v[210:213], v[10:13]
	s_setprio 0
	s_setprio 1
	v_mfma_f32_16x16x32_bf16 v[54:57], v[162:165], v[182:185], v[54:57]
	v_mfma_f32_16x16x32_bf16 v[50:53], v[174:177], v[182:185], v[50:53]
	v_mfma_f32_16x16x32_bf16 v[38:41], v[162:165], v[190:193], v[38:41]
	v_mfma_f32_16x16x32_bf16 v[34:37], v[174:177], v[190:193], v[34:37]
	v_mfma_f32_16x16x32_bf16 v[22:25], v[162:165], v[198:201], v[22:25]
	v_mfma_f32_16x16x32_bf16 v[18:21], v[174:177], v[198:201], v[18:21]
	v_mfma_f32_16x16x32_bf16 v[6:9], v[162:165], v[206:209], v[6:9]
	v_mfma_f32_16x16x32_bf16 v[2:5], v[174:177], v[206:209], v[2:5]
	v_mfma_f32_16x16x32_bf16 v[54:57], v[170:173], v[186:189], v[54:57]
	v_mfma_f32_16x16x32_bf16 v[50:53], v[178:181], v[186:189], v[50:53]
	v_mfma_f32_16x16x32_bf16 v[38:41], v[170:173], v[194:197], v[38:41]
	v_mfma_f32_16x16x32_bf16 v[34:37], v[178:181], v[194:197], v[34:37]
	v_mfma_f32_16x16x32_bf16 v[22:25], v[170:173], v[202:205], v[22:25]
	v_mfma_f32_16x16x32_bf16 v[18:21], v[178:181], v[202:205], v[18:21]
	v_mfma_f32_16x16x32_bf16 v[6:9], v[170:173], v[210:213], v[6:9]
	v_mfma_f32_16x16x32_bf16 v[2:5], v[178:181], v[210:213], v[2:5]
	s_setprio 0
	s_add_u32 s64, s64, 0x100
	s_addc_u32 s65, s65, 0
	s_add_u32 s52, s52, 0x100
	s_addc_u32 s53, s53, 0
	s_cmp_ge_i32 s66, s1
	s_mov_b32 s54, s66
	s_cbranch_scc1 .Lq4skip_ph12
	s_barrier
	s_branch .LBB0_1438
.Lq4skip_ph12:
	s_nop 1
	s_mov_b64 s[70:71], 0xe800800
	v_mov_b32_e32 v209, v1
	s_and_b64 vcc, exec, s[34:35]
	s_cbranch_vccz .LBB0_1441

.LBB0_1693:
	s_add_i32 s91, s91, 2
	s_add_u32 s64, s70, 0x100
	s_addc_u32 s65, s71, 0
	s_and_b64 s[74:75], s[68:69], exec
	s_cselect_b32 s74, 0, s64
	s_cselect_b32 s75, 0, s65
	s_add_u32 s74, s28, s74
	s_addc_u32 s75, s29, s75
	s_add_u32 s92, s51, s70
	s_addc_u32 s93, s53, s71
	s_and_b64 s[68:69], s[68:69], exec
	s_cselect_b32 s69, s55, s93
	s_cselect_b32 s68, s54, s92
	s_add_i32 s93, 0, 0x10000
	s_add_i32 s92, 0, 0x14000
	v_add_u32_e32 v2, s93, v210
	v_add_u32_e32 v6, s92, v210
	ds_read_b128 v[26:29], v2
	ds_read_b128 v[30:33], v2 offset:1024
	ds_read_b128 v[18:21], v2 offset:2048
	ds_read_b128 v[22:25], v2 offset:3072
	ds_read_b128 v[10:13], v6
	ds_read_b128 v[14:17], v6 offset:1024
	ds_read_b128 v[2:5], v6 offset:2048
	ds_read_b128 v[6:9], v6 offset:3072
	v_lshl_add_u64 v[170:171], v[194:195], 0, s[70:71]
	s_add_i32 m0, s59, 0xc000
	ds_read_b128 v[196:199], v212
	ds_read_b128 v[200:203], v212 offset:1024
	ds_read_b128 v[214:217], v212 offset:2048
	ds_read_b128 v[218:221], v212 offset:3072
	ds_read_b128 v[236:239], v212 offset:4096
	ds_read_b128 v[240:243], v212 offset:5120
	ds_read_b128 v[244:247], v212 offset:6144
	ds_read_b128 v[248:251], v212 offset:7168
	global_load_lds_dwordx4 v[170:171], off
	v_lshl_add_u64 v[170:171], v[192:193], 0, s[70:71]
	s_add_i32 m0, s59, 0xe000
	s_nop 0
	global_load_lds_dwordx4 v[170:171], off
	s_waitcnt vmcnt(8)
	s_waitcnt lgkmcnt(0)
	s_barrier
	s_setprio 1
	s_waitcnt lgkmcnt(0)
	v_mfma_scale_f32_16x16x128_f8f6f4 v[154:157], v[26:33], v[196:203], v[154:157], v208, v207 op_sel_hi:[0,0,0]
	v_mfma_scale_f32_16x16x128_f8f6f4 v[150:153], v[18:25], v[196:203], v[150:153], v208, v207 op_sel_hi:[0,0,0]
	v_mfma_scale_f32_16x16x128_f8f6f4 v[142:145], v[26:33], v[214:221], v[142:145], v208, v207 op_sel_hi:[0,0,0]
	v_mfma_scale_f32_16x16x128_f8f6f4 v[134:137], v[18:25], v[214:221], v[134:137], v208, v207 op_sel_hi:[0,0,0]
	v_mfma_scale_f32_16x16x128_f8f6f4 v[126:129], v[26:33], v[236:243], v[126:129], v208, v207 op_sel_hi:[0,0,0]
	v_mfma_scale_f32_16x16x128_f8f6f4 v[118:121], v[18:25], v[236:243], v[118:121], v208, v207 op_sel_hi:[0,0,0]
	v_mfma_scale_f32_16x16x128_f8f6f4 v[110:113], v[26:33], v[244:251], v[110:113], v208, v207 op_sel_hi:[0,0,0]
	v_mfma_scale_f32_16x16x128_f8f6f4 v[102:105], v[18:25], v[244:251], v[102:105], v208, v207 op_sel_hi:[0,0,0]
	s_setprio 0
	s_setprio 1
	v_mfma_scale_f32_16x16x128_f8f6f4 v[158:161], v[10:17], v[196:203], v[158:161], v208, v207 op_sel_hi:[0,0,0]
	v_mfma_scale_f32_16x16x128_f8f6f4 v[146:149], v[2:9], v[196:203], v[146:149], v208, v207 op_sel_hi:[0,0,0]
	v_mfma_scale_f32_16x16x128_f8f6f4 v[138:141], v[10:17], v[214:221], v[138:141], v208, v207 op_sel_hi:[0,0,0]
	v_mfma_scale_f32_16x16x128_f8f6f4 v[130:133], v[2:9], v[214:221], v[130:133], v208, v207 op_sel_hi:[0,0,0]
	v_mfma_scale_f32_16x16x128_f8f6f4 v[122:125], v[10:17], v[236:243], v[122:125], v208, v207 op_sel_hi:[0,0,0]
	v_mfma_scale_f32_16x16x128_f8f6f4 v[114:117], v[2:9], v[236:243], v[114:117], v208, v207 op_sel_hi:[0,0,0]
	v_mfma_scale_f32_16x16x128_f8f6f4 v[106:109], v[10:17], v[244:251], v[106:109], v208, v207 op_sel_hi:[0,0,0]
	v_mfma_scale_f32_16x16x128_f8f6f4 v[98:101], v[2:9], v[244:251], v[98:101], v208, v207 op_sel_hi:[0,0,0]
	s_setprio 0
	s_barrier
	s_add_i32 s70, s93, s72
	v_lshl_add_u64 v[196:197], s[68:69], 0, v[162:163]
	s_mov_b32 m0, s70
	ds_read_b128 v[214:217], v212 offset:16384
	ds_read_b128 v[218:221], v212 offset:17408
	ds_read_b128 v[236:239], v212 offset:18432
	ds_read_b128 v[240:243], v212 offset:19456
	ds_read_b128 v[244:247], v212 offset:20480
	ds_read_b128 v[248:251], v212 offset:21504
	ds_read_b128 v[170:173], v212 offset:22528
	ds_read_b128 v[174:177], v212 offset:23552
	global_load_lds_dwordx4 v[196:197], off
	s_add_i32 m0, s70, 0x2000
	s_add_u32 s70, s68, 0x20000
	v_lshl_add_u64 v[198:199], s[68:69], 0, v[164:165]
	s_addc_u32 s71, s69, 0
	s_add_i32 s92, s92, s72
	global_load_lds_dwordx4 v[198:199], off
	v_lshl_add_u64 v[200:201], s[70:71], 0, v[162:163]
	s_mov_b32 m0, s92
	v_mov_b32_e32 v179, v167
	global_load_lds_dwordx4 v[200:201], off
	v_lshl_add_u64 v[200:201], s[70:71], 0, v[164:165]
	s_add_i32 m0, s92, 0x2000
	v_lshl_add_u64 v[202:203], s[74:75], 0, v[166:167]
	global_load_lds_dwordx4 v[200:201], off
	s_mov_b32 m0, s59
	v_lshl_add_u64 v[200:201], s[74:75], 0, v[178:179]
	global_load_lds_dwordx4 v166, s[74:75]
	s_mov_b32 m0, s61
	s_nop 0
	global_load_lds_dwordx4 v178, s[74:75]
	s_waitcnt vmcnt(8)
	s_waitcnt lgkmcnt(0)
	s_barrier
	s_setprio 1
	s_waitcnt lgkmcnt(0)
	v_mfma_scale_f32_16x16x128_f8f6f4 v[94:97], v[26:33], v[214:221], v[94:97], v208, v207 op_sel_hi:[0,0,0]
	v_mfma_scale_f32_16x16x128_f8f6f4 v[86:89], v[18:25], v[214:221], v[86:89], v208, v207 op_sel_hi:[0,0,0]
	v_mfma_scale_f32_16x16x128_f8f6f4 v[78:81], v[26:33], v[236:243], v[78:81], v208, v207 op_sel_hi:[0,0,0]
	v_mfma_scale_f32_16x16x128_f8f6f4 v[70:73], v[18:25], v[236:243], v[70:73], v208, v207 op_sel_hi:[0,0,0]
	v_mfma_scale_f32_16x16x128_f8f6f4 v[62:65], v[26:33], v[244:251], v[62:65], v208, v207 op_sel_hi:[0,0,0]
	v_mfma_scale_f32_16x16x128_f8f6f4 v[54:57], v[18:25], v[244:251], v[54:57], v208, v207 op_sel_hi:[0,0,0]
	v_mfma_scale_f32_16x16x128_f8f6f4 v[46:49], v[26:33], v[170:177], v[46:49], v208, v207 op_sel_hi:[0,0,0]
	v_mfma_scale_f32_16x16x128_f8f6f4 v[38:41], v[18:25], v[170:177], v[38:41], v208, v207 op_sel_hi:[0,0,0]
	s_setprio 0
	s_setprio 1
	v_mfma_scale_f32_16x16x128_f8f6f4 v[90:93], v[10:17], v[214:221], v[90:93], v208, v207 op_sel_hi:[0,0,0]
	v_mfma_scale_f32_16x16x128_f8f6f4 v[82:85], v[2:9], v[214:221], v[82:85], v208, v207 op_sel_hi:[0,0,0]
	v_mfma_scale_f32_16x16x128_f8f6f4 v[74:77], v[10:17], v[236:243], v[74:77], v208, v207 op_sel_hi:[0,0,0]
	v_mfma_scale_f32_16x16x128_f8f6f4 v[66:69], v[2:9], v[236:243], v[66:69], v208, v207 op_sel_hi:[0,0,0]
	v_mfma_scale_f32_16x16x128_f8f6f4 v[58:61], v[10:17], v[244:251], v[58:61], v208, v207 op_sel_hi:[0,0,0]
	v_mfma_scale_f32_16x16x128_f8f6f4 v[50:53], v[2:9], v[244:251], v[50:53], v208, v207 op_sel_hi:[0,0,0]
	v_mfma_scale_f32_16x16x128_f8f6f4 v[42:45], v[10:17], v[170:177], v[42:45], v208, v207 op_sel_hi:[0,0,0]
	v_mfma_scale_f32_16x16x128_f8f6f4 v[34:37], v[2:9], v[170:177], v[34:37], v208, v207 op_sel_hi:[0,0,0]
	s_setprio 0
	s_barrier
	s_add_i32 s70, 0, 0x18000
	s_add_i32 s71, 0, 0x1c000
	v_add_u32_e32 v2, s70, v210
	v_add_u32_e32 v6, s71, v210
	ds_read_b128 v[26:29], v2
	ds_read_b128 v[30:33], v2 offset:1024
	ds_read_b128 v[18:21], v2 offset:2048
	ds_read_b128 v[22:25], v2 offset:3072
	ds_read_b128 v[10:13], v6
	ds_read_b128 v[14:17], v6 offset:1024
	ds_read_b128 v[2:5], v6 offset:2048
	ds_read_b128 v[6:9], v6 offset:3072
	s_mov_b32 m0, s73
	ds_read_b128 v[170:173], v212 offset:32768
	ds_read_b128 v[174:177], v212 offset:33792
	ds_read_b128 v[214:217], v212 offset:34816
	ds_read_b128 v[218:221], v212 offset:35840
	ds_read_b128 v[236:239], v212 offset:36864
	ds_read_b128 v[240:243], v212 offset:37888
	ds_read_b128 v[244:247], v212 offset:38912
	ds_read_b128 v[248:251], v212 offset:39936
	global_load_lds_dwordx4 v180, s[74:75]
	s_mov_b32 m0, s76
	s_nop 0
	global_load_lds_dwordx4 v182, s[74:75]
	s_waitcnt vmcnt(8)
	s_waitcnt lgkmcnt(0)
	s_barrier
	s_setprio 1
	s_waitcnt lgkmcnt(0)
	v_mfma_scale_f32_16x16x128_f8f6f4 v[154:157], v[26:33], v[170:177], v[154:157], v208, v207 op_sel_hi:[0,0,0]
	v_mfma_scale_f32_16x16x128_f8f6f4 v[150:153], v[18:25], v[170:177], v[150:153], v208, v207 op_sel_hi:[0,0,0]
	v_mfma_scale_f32_16x16x128_f8f6f4 v[142:145], v[26:33], v[214:221], v[142:145], v208, v207 op_sel_hi:[0,0,0]
	v_mfma_scale_f32_16x16x128_f8f6f4 v[134:137], v[18:25], v[214:221], v[134:137], v208, v207 op_sel_hi:[0,0,0]
	v_mfma_scale_f32_16x16x128_f8f6f4 v[126:129], v[26:33], v[236:243], v[126:129], v208, v207 op_sel_hi:[0,0,0]
	v_mfma_scale_f32_16x16x128_f8f6f4 v[118:121], v[18:25], v[236:243], v[118:121], v208, v207 op_sel_hi:[0,0,0]
	v_mfma_scale_f32_16x16x128_f8f6f4 v[110:113], v[26:33], v[244:251], v[110:113], v208, v207 op_sel_hi:[0,0,0]
	v_mfma_scale_f32_16x16x128_f8f6f4 v[102:105], v[18:25], v[244:251], v[102:105], v208, v207 op_sel_hi:[0,0,0]
	s_setprio 0
	s_setprio 1
	v_mfma_scale_f32_16x16x128_f8f6f4 v[158:161], v[10:17], v[170:177], v[158:161], v208, v207 op_sel_hi:[0,0,0]
	v_mfma_scale_f32_16x16x128_f8f6f4 v[146:149], v[2:9], v[170:177], v[146:149], v208, v207 op_sel_hi:[0,0,0]
	v_mfma_scale_f32_16x16x128_f8f6f4 v[138:141], v[10:17], v[214:221], v[138:141], v208, v207 op_sel_hi:[0,0,0]
	v_mfma_scale_f32_16x16x128_f8f6f4 v[130:133], v[2:9], v[214:221], v[130:133], v208, v207 op_sel_hi:[0,0,0]
	v_mfma_scale_f32_16x16x128_f8f6f4 v[122:125], v[10:17], v[236:243], v[122:125], v208, v207 op_sel_hi:[0,0,0]
	v_mfma_scale_f32_16x16x128_f8f6f4 v[114:117], v[2:9], v[236:243], v[114:117], v208, v207 op_sel_hi:[0,0,0]
	v_mfma_scale_f32_16x16x128_f8f6f4 v[106:109], v[10:17], v[244:251], v[106:109], v208, v207 op_sel_hi:[0,0,0]
	v_mfma_scale_f32_16x16x128_f8f6f4 v[98:101], v[2:9], v[244:251], v[98:101], v208, v207 op_sel_hi:[0,0,0]
	s_setprio 0
	s_barrier
	s_add_i32 s70, s70, s72
	v_lshl_add_u64 v[196:197], v[196:197], 0, s[56:57]
	s_mov_b32 m0, s70
	ds_read_b128 v[170:173], v212 offset:49152
	ds_read_b128 v[174:177], v212 offset:50176
	ds_read_b128 v[214:217], v212 offset:51200
	ds_read_b128 v[218:221], v212 offset:52224
	ds_read_b128 v[236:239], v212 offset:53248
	ds_read_b128 v[240:243], v212 offset:54272
	ds_read_b128 v[244:247], v212 offset:55296
	ds_read_b128 v[248:251], v212 offset:56320
	global_load_lds_dwordx4 v[196:197], off
	s_add_i32 m0, s70, 0x2000
	s_add_u32 s68, s68, 0x20080
	v_lshl_add_u64 v[196:197], v[198:199], 0, s[56:57]
	s_addc_u32 s69, s69, 0
	s_add_i32 s70, s71, s72
	global_load_lds_dwordx4 v[196:197], off
	v_lshl_add_u64 v[196:197], s[68:69], 0, v[162:163]
	s_mov_b32 m0, s70
	s_nop 0
	global_load_lds_dwordx4 v[196:197], off
	v_lshl_add_u64 v[196:197], s[68:69], 0, v[164:165]
	s_add_i32 m0, s70, 0x2000
	s_nop 0
	global_load_lds_dwordx4 v[196:197], off
	v_lshl_add_u64 v[196:197], v[202:203], 0, s[56:57]
	s_mov_b32 m0, s77
	s_nop 0
	global_load_lds_dwordx4 v[196:197], off
	v_lshl_add_u64 v[196:197], v[200:201], 0, s[56:57]
	s_mov_b32 m0, s79
	s_nop 0
	global_load_lds_dwordx4 v[196:197], off
	s_waitcnt vmcnt(8)
	s_waitcnt lgkmcnt(0)
	s_barrier
	s_setprio 1
	s_waitcnt lgkmcnt(0)
	v_mfma_scale_f32_16x16x128_f8f6f4 v[94:97], v[26:33], v[170:177], v[94:97], v208, v207 op_sel_hi:[0,0,0]
	v_mfma_scale_f32_16x16x128_f8f6f4 v[86:89], v[18:25], v[170:177], v[86:89], v208, v207 op_sel_hi:[0,0,0]
	v_mfma_scale_f32_16x16x128_f8f6f4 v[78:81], v[26:33], v[214:221], v[78:81], v208, v207 op_sel_hi:[0,0,0]
	v_mfma_scale_f32_16x16x128_f8f6f4 v[70:73], v[18:25], v[214:221], v[70:73], v208, v207 op_sel_hi:[0,0,0]
	v_mfma_scale_f32_16x16x128_f8f6f4 v[62:65], v[26:33], v[236:243], v[62:65], v208, v207 op_sel_hi:[0,0,0]
	v_mfma_scale_f32_16x16x128_f8f6f4 v[54:57], v[18:25], v[236:243], v[54:57], v208, v207 op_sel_hi:[0,0,0]
	v_mfma_scale_f32_16x16x128_f8f6f4 v[46:49], v[26:33], v[244:251], v[46:49], v208, v207 op_sel_hi:[0,0,0]
	v_mfma_scale_f32_16x16x128_f8f6f4 v[38:41], v[18:25], v[244:251], v[38:41], v208, v207 op_sel_hi:[0,0,0]
	s_setprio 0
	s_setprio 1
	v_mfma_scale_f32_16x16x128_f8f6f4 v[90:93], v[10:17], v[170:177], v[90:93], v208, v207 op_sel_hi:[0,0,0]
	v_mfma_scale_f32_16x16x128_f8f6f4 v[82:85], v[2:9], v[170:177], v[82:85], v208, v207 op_sel_hi:[0,0,0]
	v_mfma_scale_f32_16x16x128_f8f6f4 v[74:77], v[10:17], v[214:221], v[74:77], v208, v207 op_sel_hi:[0,0,0]
	v_mfma_scale_f32_16x16x128_f8f6f4 v[66:69], v[2:9], v[214:221], v[66:69], v208, v207 op_sel_hi:[0,0,0]
	v_mfma_scale_f32_16x16x128_f8f6f4 v[58:61], v[10:17], v[236:243], v[58:61], v208, v207 op_sel_hi:[0,0,0]
	v_mfma_scale_f32_16x16x128_f8f6f4 v[50:53], v[2:9], v[236:243], v[50:53], v208, v207 op_sel_hi:[0,0,0]
	v_mfma_scale_f32_16x16x128_f8f6f4 v[42:45], v[10:17], v[244:251], v[42:45], v208, v207 op_sel_hi:[0,0,0]
	v_mfma_scale_f32_16x16x128_f8f6f4 v[34:37], v[2:9], v[244:251], v[34:37], v208, v207 op_sel_hi:[0,0,0]
	s_setprio 0
	s_cmp_ge_i32 s91, s11
	s_cbranch_scc1 .LBB0_1695
	s_barrier
	s_mov_b64 s[70:71], s[64:65]
	s_branch .LBB0_1691
.LBB0_1695:
	s_nop 1
	s_movk_i32 s93, 0x1000
	s_mov_b64 s[70:71], 0xe800800
	s_and_b64 vcc, exec, s[44:45]
	s_cbranch_vccz .LBB0_1697

.LBB0_1838:
	s_add_i32 s55, s55, 2
	s_add_u32 s60, s64, 0x100
	s_addc_u32 s61, s65, 0
	s_and_b64 s[68:69], s[62:63], exec
	s_cselect_b32 s68, 0, s60
	s_cselect_b32 s69, 0, s61
	s_add_u32 s68, s30, s68
	s_addc_u32 s69, s31, s69
	s_add_u32 s91, s47, s64
	s_addc_u32 s92, s49, s65
	s_and_b64 s[62:63], s[62:63], exec
	s_cselect_b32 s63, s53, s92
	s_cselect_b32 s62, s52, s91
	s_add_i32 s92, 0, 0x10000
	s_add_i32 s91, 0, 0x14000
	v_add_u32_e32 v2, s92, v210
	v_add_u32_e32 v6, s91, v210
	ds_read_b128 v[26:29], v2
	ds_read_b128 v[30:33], v2 offset:1024
	ds_read_b128 v[18:21], v2 offset:2048
	ds_read_b128 v[22:25], v2 offset:3072
	ds_read_b128 v[10:13], v6
	ds_read_b128 v[14:17], v6 offset:1024
	ds_read_b128 v[2:5], v6 offset:2048
	ds_read_b128 v[6:9], v6 offset:3072
	v_lshl_add_u64 v[222:223], v[194:195], 0, s[64:65]
	s_add_i32 m0, s59, 0xc000
	ds_read_b128 v[170:173], v212
	ds_read_b128 v[174:177], v212 offset:1024
	ds_read_b128 v[196:199], v212 offset:2048
	ds_read_b128 v[200:203], v212 offset:3072
	ds_read_b128 v[214:217], v212 offset:4096
	ds_read_b128 v[218:221], v212 offset:5120
	ds_read_b128 v[236:239], v212 offset:6144
	ds_read_b128 v[240:243], v212 offset:7168
	global_load_lds_dwordx4 v[222:223], off
	v_lshl_add_u64 v[222:223], v[192:193], 0, s[64:65]
	s_add_i32 m0, s59, 0xe000
	s_nop 0
	global_load_lds_dwordx4 v[222:223], off
	s_waitcnt vmcnt(8)
	s_waitcnt lgkmcnt(0)
	s_barrier
	s_setprio 1
	s_waitcnt lgkmcnt(0)
	v_mfma_scale_f32_16x16x128_f8f6f4 v[154:157], v[26:33], v[170:177], v[154:157], v208, v207 op_sel_hi:[0,0,0]
	v_mfma_scale_f32_16x16x128_f8f6f4 v[150:153], v[18:25], v[170:177], v[150:153], v208, v207 op_sel_hi:[0,0,0]
	v_mfma_scale_f32_16x16x128_f8f6f4 v[142:145], v[26:33], v[196:203], v[142:145], v208, v207 op_sel_hi:[0,0,0]
	v_mfma_scale_f32_16x16x128_f8f6f4 v[134:137], v[18:25], v[196:203], v[134:137], v208, v207 op_sel_hi:[0,0,0]
	v_mfma_scale_f32_16x16x128_f8f6f4 v[126:129], v[26:33], v[214:221], v[126:129], v208, v207 op_sel_hi:[0,0,0]
	v_mfma_scale_f32_16x16x128_f8f6f4 v[118:121], v[18:25], v[214:221], v[118:121], v208, v207 op_sel_hi:[0,0,0]
	v_mfma_scale_f32_16x16x128_f8f6f4 v[110:113], v[26:33], v[236:243], v[110:113], v208, v207 op_sel_hi:[0,0,0]
	v_mfma_scale_f32_16x16x128_f8f6f4 v[102:105], v[18:25], v[236:243], v[102:105], v208, v207 op_sel_hi:[0,0,0]
	s_setprio 0
	s_setprio 1
	v_mfma_scale_f32_16x16x128_f8f6f4 v[158:161], v[10:17], v[170:177], v[158:161], v208, v207 op_sel_hi:[0,0,0]
	v_mfma_scale_f32_16x16x128_f8f6f4 v[146:149], v[2:9], v[170:177], v[146:149], v208, v207 op_sel_hi:[0,0,0]
	v_mfma_scale_f32_16x16x128_f8f6f4 v[138:141], v[10:17], v[196:203], v[138:141], v208, v207 op_sel_hi:[0,0,0]
	v_mfma_scale_f32_16x16x128_f8f6f4 v[130:133], v[2:9], v[196:203], v[130:133], v208, v207 op_sel_hi:[0,0,0]
	v_mfma_scale_f32_16x16x128_f8f6f4 v[122:125], v[10:17], v[214:221], v[122:125], v208, v207 op_sel_hi:[0,0,0]
	v_mfma_scale_f32_16x16x128_f8f6f4 v[114:117], v[2:9], v[214:221], v[114:117], v208, v207 op_sel_hi:[0,0,0]
	v_mfma_scale_f32_16x16x128_f8f6f4 v[106:109], v[10:17], v[236:243], v[106:109], v208, v207 op_sel_hi:[0,0,0]
	v_mfma_scale_f32_16x16x128_f8f6f4 v[98:101], v[2:9], v[236:243], v[98:101], v208, v207 op_sel_hi:[0,0,0]
	s_setprio 0
	s_barrier
	s_add_i32 s64, s92, s22
	v_lshl_add_u64 v[196:197], s[62:63], 0, v[162:163]
	s_mov_b32 m0, s64
	ds_read_b128 v[170:173], v212 offset:16384
	ds_read_b128 v[174:177], v212 offset:17408
	ds_read_b128 v[214:217], v212 offset:18432
	ds_read_b128 v[218:221], v212 offset:19456
	ds_read_b128 v[236:239], v212 offset:20480
	ds_read_b128 v[240:243], v212 offset:21504
	ds_read_b128 v[244:247], v212 offset:22528
	ds_read_b128 v[248:251], v212 offset:23552
	global_load_lds_dwordx4 v[196:197], off
	s_add_i32 m0, s64, 0x2000
	s_add_u32 s64, s62, 0x20000
	v_lshl_add_u64 v[198:199], s[62:63], 0, v[164:165]
	s_addc_u32 s65, s63, 0
	s_add_i32 s91, s91, s22
	global_load_lds_dwordx4 v[198:199], off
	v_lshl_add_u64 v[200:201], s[64:65], 0, v[162:163]
	s_mov_b32 m0, s91
	v_mov_b32_e32 v179, v167
	global_load_lds_dwordx4 v[200:201], off
	v_lshl_add_u64 v[200:201], s[64:65], 0, v[164:165]
	s_add_i32 m0, s91, 0x2000
	v_lshl_add_u64 v[202:203], s[68:69], 0, v[166:167]
	global_load_lds_dwordx4 v[200:201], off
	s_mov_b32 m0, s59
	v_lshl_add_u64 v[200:201], s[68:69], 0, v[178:179]
	global_load_lds_dwordx4 v166, s[68:69]
	s_mov_b32 m0, s71
	s_nop 0
	global_load_lds_dwordx4 v178, s[68:69]
	s_waitcnt vmcnt(8)
	s_waitcnt lgkmcnt(0)
	s_barrier
	s_setprio 1
	s_waitcnt lgkmcnt(0)
	v_mfma_scale_f32_16x16x128_f8f6f4 v[94:97], v[26:33], v[170:177], v[94:97], v208, v207 op_sel_hi:[0,0,0]
	v_mfma_scale_f32_16x16x128_f8f6f4 v[86:89], v[18:25], v[170:177], v[86:89], v208, v207 op_sel_hi:[0,0,0]
	v_mfma_scale_f32_16x16x128_f8f6f4 v[78:81], v[26:33], v[214:221], v[78:81], v208, v207 op_sel_hi:[0,0,0]
	v_mfma_scale_f32_16x16x128_f8f6f4 v[70:73], v[18:25], v[214:221], v[70:73], v208, v207 op_sel_hi:[0,0,0]
	v_mfma_scale_f32_16x16x128_f8f6f4 v[62:65], v[26:33], v[236:243], v[62:65], v208, v207 op_sel_hi:[0,0,0]
	v_mfma_scale_f32_16x16x128_f8f6f4 v[54:57], v[18:25], v[236:243], v[54:57], v208, v207 op_sel_hi:[0,0,0]
	v_mfma_scale_f32_16x16x128_f8f6f4 v[46:49], v[26:33], v[244:251], v[46:49], v208, v207 op_sel_hi:[0,0,0]
	v_mfma_scale_f32_16x16x128_f8f6f4 v[38:41], v[18:25], v[244:251], v[38:41], v208, v207 op_sel_hi:[0,0,0]
	s_setprio 0
	s_setprio 1
	v_mfma_scale_f32_16x16x128_f8f6f4 v[90:93], v[10:17], v[170:177], v[90:93], v208, v207 op_sel_hi:[0,0,0]
	v_mfma_scale_f32_16x16x128_f8f6f4 v[82:85], v[2:9], v[170:177], v[82:85], v208, v207 op_sel_hi:[0,0,0]
	v_mfma_scale_f32_16x16x128_f8f6f4 v[74:77], v[10:17], v[214:221], v[74:77], v208, v207 op_sel_hi:[0,0,0]
	v_mfma_scale_f32_16x16x128_f8f6f4 v[66:69], v[2:9], v[214:221], v[66:69], v208, v207 op_sel_hi:[0,0,0]
	v_mfma_scale_f32_16x16x128_f8f6f4 v[58:61], v[10:17], v[236:243], v[58:61], v208, v207 op_sel_hi:[0,0,0]
	v_mfma_scale_f32_16x16x128_f8f6f4 v[50:53], v[2:9], v[236:243], v[50:53], v208, v207 op_sel_hi:[0,0,0]
	v_mfma_scale_f32_16x16x128_f8f6f4 v[42:45], v[10:17], v[244:251], v[42:45], v208, v207 op_sel_hi:[0,0,0]
	v_mfma_scale_f32_16x16x128_f8f6f4 v[34:37], v[2:9], v[244:251], v[34:37], v208, v207 op_sel_hi:[0,0,0]
	s_setprio 0
	s_barrier
	s_add_i32 s64, 0, 0x18000
	s_add_i32 s65, 0, 0x1c000
	v_add_u32_e32 v2, s64, v210
	v_add_u32_e32 v6, s65, v210
	ds_read_b128 v[26:29], v2
	ds_read_b128 v[30:33], v2 offset:1024
	ds_read_b128 v[18:21], v2 offset:2048
	ds_read_b128 v[22:25], v2 offset:3072
	ds_read_b128 v[10:13], v6
	ds_read_b128 v[14:17], v6 offset:1024
	ds_read_b128 v[2:5], v6 offset:2048
	ds_read_b128 v[6:9], v6 offset:3072
	s_mov_b32 m0, s72
	ds_read_b128 v[170:173], v212 offset:32768
	ds_read_b128 v[174:177], v212 offset:33792
	ds_read_b128 v[214:217], v212 offset:34816
	ds_read_b128 v[218:221], v212 offset:35840
	ds_read_b128 v[236:239], v212 offset:36864
	ds_read_b128 v[240:243], v212 offset:37888
	ds_read_b128 v[244:247], v212 offset:38912
	ds_read_b128 v[248:251], v212 offset:39936
	global_load_lds_dwordx4 v180, s[68:69]
	s_mov_b32 m0, s73
	s_nop 0
	global_load_lds_dwordx4 v182, s[68:69]
	s_waitcnt vmcnt(8)
	s_waitcnt lgkmcnt(0)
	s_barrier
	s_setprio 1
	s_waitcnt lgkmcnt(0)
	v_mfma_scale_f32_16x16x128_f8f6f4 v[154:157], v[26:33], v[170:177], v[154:157], v208, v207 op_sel_hi:[0,0,0]
	v_mfma_scale_f32_16x16x128_f8f6f4 v[150:153], v[18:25], v[170:177], v[150:153], v208, v207 op_sel_hi:[0,0,0]
	v_mfma_scale_f32_16x16x128_f8f6f4 v[142:145], v[26:33], v[214:221], v[142:145], v208, v207 op_sel_hi:[0,0,0]
	v_mfma_scale_f32_16x16x128_f8f6f4 v[134:137], v[18:25], v[214:221], v[134:137], v208, v207 op_sel_hi:[0,0,0]
	v_mfma_scale_f32_16x16x128_f8f6f4 v[126:129], v[26:33], v[236:243], v[126:129], v208, v207 op_sel_hi:[0,0,0]
	v_mfma_scale_f32_16x16x128_f8f6f4 v[118:121], v[18:25], v[236:243], v[118:121], v208, v207 op_sel_hi:[0,0,0]
	v_mfma_scale_f32_16x16x128_f8f6f4 v[110:113], v[26:33], v[244:251], v[110:113], v208, v207 op_sel_hi:[0,0,0]
	v_mfma_scale_f32_16x16x128_f8f6f4 v[102:105], v[18:25], v[244:251], v[102:105], v208, v207 op_sel_hi:[0,0,0]
	s_setprio 0
	s_setprio 1
	v_mfma_scale_f32_16x16x128_f8f6f4 v[158:161], v[10:17], v[170:177], v[158:161], v208, v207 op_sel_hi:[0,0,0]
	v_mfma_scale_f32_16x16x128_f8f6f4 v[146:149], v[2:9], v[170:177], v[146:149], v208, v207 op_sel_hi:[0,0,0]
	v_mfma_scale_f32_16x16x128_f8f6f4 v[138:141], v[10:17], v[214:221], v[138:141], v208, v207 op_sel_hi:[0,0,0]
	v_mfma_scale_f32_16x16x128_f8f6f4 v[130:133], v[2:9], v[214:221], v[130:133], v208, v207 op_sel_hi:[0,0,0]
	v_mfma_scale_f32_16x16x128_f8f6f4 v[122:125], v[10:17], v[236:243], v[122:125], v208, v207 op_sel_hi:[0,0,0]
	v_mfma_scale_f32_16x16x128_f8f6f4 v[114:117], v[2:9], v[236:243], v[114:117], v208, v207 op_sel_hi:[0,0,0]
	v_mfma_scale_f32_16x16x128_f8f6f4 v[106:109], v[10:17], v[244:251], v[106:109], v208, v207 op_sel_hi:[0,0,0]
	v_mfma_scale_f32_16x16x128_f8f6f4 v[98:101], v[2:9], v[244:251], v[98:101], v208, v207 op_sel_hi:[0,0,0]
	s_setprio 0
	s_barrier
	s_add_i32 s64, s64, s22
	v_lshl_add_u64 v[196:197], v[196:197], 0, s[56:57]
	s_mov_b32 m0, s64
	ds_read_b128 v[170:173], v212 offset:49152
	ds_read_b128 v[174:177], v212 offset:50176
	ds_read_b128 v[214:217], v212 offset:51200
	ds_read_b128 v[218:221], v212 offset:52224
	ds_read_b128 v[236:239], v212 offset:53248
	ds_read_b128 v[240:243], v212 offset:54272
	ds_read_b128 v[244:247], v212 offset:55296
	ds_read_b128 v[248:251], v212 offset:56320
	global_load_lds_dwordx4 v[196:197], off
	s_add_i32 m0, s64, 0x2000
	s_add_u32 s62, s62, 0x20080
	v_lshl_add_u64 v[196:197], v[198:199], 0, s[56:57]
	s_addc_u32 s63, s63, 0
	s_add_i32 s64, s65, s22
	global_load_lds_dwordx4 v[196:197], off
	v_lshl_add_u64 v[196:197], s[62:63], 0, v[162:163]
	s_mov_b32 m0, s64
	s_nop 0
	global_load_lds_dwordx4 v[196:197], off
	v_lshl_add_u64 v[196:197], s[62:63], 0, v[164:165]
	s_add_i32 m0, s64, 0x2000
	s_nop 0
	global_load_lds_dwordx4 v[196:197], off
	v_lshl_add_u64 v[196:197], v[202:203], 0, s[56:57]
	s_mov_b32 m0, s74
	s_nop 0
	global_load_lds_dwordx4 v[196:197], off
	v_lshl_add_u64 v[196:197], v[200:201], 0, s[56:57]
	s_mov_b32 m0, s75
	s_nop 0
	global_load_lds_dwordx4 v[196:197], off
	s_waitcnt vmcnt(8)
	s_waitcnt lgkmcnt(0)
	s_barrier
	s_setprio 1
	s_waitcnt lgkmcnt(0)
	v_mfma_scale_f32_16x16x128_f8f6f4 v[94:97], v[26:33], v[170:177], v[94:97], v208, v207 op_sel_hi:[0,0,0]
	v_mfma_scale_f32_16x16x128_f8f6f4 v[86:89], v[18:25], v[170:177], v[86:89], v208, v207 op_sel_hi:[0,0,0]
	v_mfma_scale_f32_16x16x128_f8f6f4 v[78:81], v[26:33], v[214:221], v[78:81], v208, v207 op_sel_hi:[0,0,0]
	v_mfma_scale_f32_16x16x128_f8f6f4 v[70:73], v[18:25], v[214:221], v[70:73], v208, v207 op_sel_hi:[0,0,0]
	v_mfma_scale_f32_16x16x128_f8f6f4 v[62:65], v[26:33], v[236:243], v[62:65], v208, v207 op_sel_hi:[0,0,0]
	v_mfma_scale_f32_16x16x128_f8f6f4 v[54:57], v[18:25], v[236:243], v[54:57], v208, v207 op_sel_hi:[0,0,0]
	v_mfma_scale_f32_16x16x128_f8f6f4 v[46:49], v[26:33], v[244:251], v[46:49], v208, v207 op_sel_hi:[0,0,0]
	v_mfma_scale_f32_16x16x128_f8f6f4 v[38:41], v[18:25], v[244:251], v[38:41], v208, v207 op_sel_hi:[0,0,0]
	s_setprio 0
	s_setprio 1
	v_mfma_scale_f32_16x16x128_f8f6f4 v[90:93], v[10:17], v[170:177], v[90:93], v208, v207 op_sel_hi:[0,0,0]
	v_mfma_scale_f32_16x16x128_f8f6f4 v[82:85], v[2:9], v[170:177], v[82:85], v208, v207 op_sel_hi:[0,0,0]
	v_mfma_scale_f32_16x16x128_f8f6f4 v[74:77], v[10:17], v[214:221], v[74:77], v208, v207 op_sel_hi:[0,0,0]
	v_mfma_scale_f32_16x16x128_f8f6f4 v[66:69], v[2:9], v[214:221], v[66:69], v208, v207 op_sel_hi:[0,0,0]
	v_mfma_scale_f32_16x16x128_f8f6f4 v[58:61], v[10:17], v[236:243], v[58:61], v208, v207 op_sel_hi:[0,0,0]
	v_mfma_scale_f32_16x16x128_f8f6f4 v[50:53], v[2:9], v[236:243], v[50:53], v208, v207 op_sel_hi:[0,0,0]
	v_mfma_scale_f32_16x16x128_f8f6f4 v[42:45], v[10:17], v[244:251], v[42:45], v208, v207 op_sel_hi:[0,0,0]
	v_mfma_scale_f32_16x16x128_f8f6f4 v[34:37], v[2:9], v[244:251], v[34:37], v208, v207 op_sel_hi:[0,0,0]
	s_setprio 0
	s_cmp_lt_i32 s55, s11
	s_cbranch_scc0 .LBB0_1841
	s_barrier
	s_mov_b64 s[64:65], s[60:61]
	s_branch .LBB0_1836

.LBB0_1841:
	s_nop 1
	s_andn2_b64 vcc, exec, s[42:43]
	s_cbranch_vccnz .LBB0_1843
	s_barrier
